# speedup vs baseline: 1.0227x; 1.0227x over previous
.Lk_15:
	global_load_dword v66, v[62:63], off offset:4
	global_load_dword v67, v[62:63], off offset:260
	global_load_dword v68, v[62:63], off offset:516
	global_load_dword v69, v[62:63], off offset:772
	global_load_dword v70, v[64:65], off offset:4
	global_load_dword v71, v[64:65], off offset:260
	global_load_dword v72, v[64:65], off offset:516
	global_load_dword v73, v[64:65], off offset:772
	v_and_b32_e32 v62, 15, v0
	s_mov_b32 s8, 0x4038aa3b
	s_waitcnt vmcnt(11)
	v_pk_mul_f32 v[38:39], v[50:51], v[38:39]
	v_lshlrev_b32_e32 v57, 2, v1
	s_lshl_b32 s10, s34, 8
	v_lshlrev_b32_e32 v1, 4, v62
	v_pk_add_f32 v[52:53], v[52:53], v[54:55]
	v_pk_add_f32 v[54:55], v[58:59], v[60:61]
	s_mov_b32 s9, 0xbfb8aa3b
	s_waitcnt vmcnt(10)
	v_pk_mul_f32 v[46:47], v[50:51], v[46:47]
	v_pk_mul_f32 v[48:49], v[50:51], v[48:49]
	v_pk_mul_f32 v[40:41], v[50:51], v[40:41]
	s_waitcnt vmcnt(8)
	v_pk_mul_f32 v[42:43], v[50:51], v[42:43]
	v_pk_mul_f32 v[44:45], v[50:51], v[44:45]
	v_pk_mul_f32 v[34:35], v[50:51], v[34:35]
	v_pk_mul_f32 v[36:37], v[50:51], v[36:37]
	v_pk_mul_f32 v[30:31], v[50:51], v[30:31]
	v_pk_mul_f32 v[32:33], v[50:51], v[32:33]
	v_pk_mul_f32 v[18:19], v[50:51], v[18:19]
	v_pk_mul_f32 v[58:59], v[50:51], v[20:21]
	v_pk_mul_f32 v[60:61], v[50:51], v[26:27]
	v_pk_mul_f32 v[64:65], v[50:51], v[28:29]
	v_pk_mul_f32 v[74:75], v[50:51], v[22:23]
	v_pk_mul_f32 v[50:51], v[50:51], v[24:25]
	v_cvt_pk_f16_f32 v24, v38, v39
	v_or3_b32 v38, v1, v57, s10
	v_lshlrev_b32_e32 v82, 4, v80
	s_and_b64 vcc, exec, s[6:7]
	s_mov_b32 s6, s9
	v_cvt_pk_f16_f32 v25, v40, v41
	v_add_u32_e32 v81, 0x23280, v38
	s_mov_b64 s[4:5], -1
	v_pk_mul_f32 v[20:21], v[54:55], s[8:9]
	v_cvt_pk_f16_f32 v22, v46, v47
	v_cvt_pk_f16_f32 v23, v48, v49
	v_cvt_pk_f16_f32 v26, v42, v43
	v_cvt_pk_f16_f32 v27, v44, v45
	v_cvt_pk_f16_f32 v28, v34, v35
	v_cvt_pk_f16_f32 v29, v36, v37
	v_cvt_pk_f16_f32 v30, v30, v31
	v_cvt_pk_f16_f32 v31, v32, v33
	v_cvt_pk_f16_f32 v32, v18, v19
	v_cvt_pk_f16_f32 v33, v58, v59
	v_cvt_pk_f16_f32 v34, v60, v61
	v_cvt_pk_f16_f32 v35, v64, v65
	v_cvt_pk_f16_f32 v36, v74, v75
	v_cvt_pk_f16_f32 v37, v50, v51
	v_add_u32_e32 v75, 0x23280, v82
	v_pk_mul_f32 v[18:19], v[52:53], s[6:7] op_sel_hi:[1,0]
	s_waitcnt lgkmcnt(0)
	s_barrier
	s_waitcnt vmcnt(2)
	v_pk_add_f32 v[38:39], v[66:67], v[70:71]
	s_nop 0
	v_pk_mul_f32 v[38:39], v[38:39], s[6:7] op_sel_hi:[1,0]
	s_waitcnt vmcnt(0)
	v_pk_add_f32 v[40:41], v[68:69], v[72:73]
	s_nop 0
	v_pk_mul_f32 v[40:41], v[40:41], s[8:9]
	s_cbranch_vccz .Lk_134
	s_setprio 0
	v_lshrrev_b32_e32 v42, 4, v80
	v_lshlrev_b32_e32 v42, 5, v42
	global_load_dwordx4 v[44:47], v42, s[18:19]
	global_load_dwordx4 v[48:51], v42, s[18:19] offset:16
	global_load_dwordx4 v[52:55], v42, s[18:19] offset:128
	global_load_dwordx4 v[56:59], v42, s[18:19] offset:144
	s_load_dword s28, s[20:21], 0x0
	v_and_b32_e32 v43, 15, v80
	v_cmp_eq_u32_e32 vcc, 1, v43
	v_cmp_eq_u32_e64 s[4:5], 0, v43
	v_cmp_gt_u32_e64 s[30:31], 16, v80
	v_lshl_or_b32 v124, s3, 4, v43
	v_mul_u32_u24_e32 v124, 0x708, v124
	v_lshlrev_b32_e32 v74, 2, v43
	v_add_u32_e32 v74, 0x1c200, v74
	v_mov_b32_e32 v92, 0xc038aa3b
	v_mov_b32_e32 v93, 0xc038aa3b
	s_mov_b32 s8, 0x4038aa3b
	s_mov_b32 s9, 0
	v_mov_b32_e32 v64, 0
	v_mov_b32_e32 v65, 0
	s_mov_b32 s12, 4
	s_waitcnt vmcnt(0) lgkmcnt(0)
	v_cvt_f16_f32_e32 v60, v44
	v_cvt_f32_f16_e32 v61, v60
	v_sub_f32_e32 v61, v44, v61
	v_cvt_f16_f32_e32 v61, v61
	v_cndmask_b32_e32 v61, 0, v61, vcc
	v_cndmask_b32_e64 v94, v61, v60, s[4:5]
	v_cvt_f16_f32_e32 v60, v45
	v_cvt_f32_f16_e32 v61, v60
	v_sub_f32_e32 v61, v45, v61
	v_cvt_f16_f32_e32 v61, v61
	v_cndmask_b32_e32 v61, 0, v61, vcc
	v_cndmask_b32_e64 v95, v61, v60, s[4:5]
	v_cvt_f16_f32_e32 v60, v46
	v_cvt_f32_f16_e32 v61, v60
	v_sub_f32_e32 v61, v46, v61
	v_cvt_f16_f32_e32 v61, v61
	v_cndmask_b32_e32 v61, 0, v61, vcc
	v_cndmask_b32_e64 v96, v61, v60, s[4:5]
	v_cvt_f16_f32_e32 v60, v47
	v_cvt_f32_f16_e32 v61, v60
	v_sub_f32_e32 v61, v47, v61
	v_cvt_f16_f32_e32 v61, v61
	v_cndmask_b32_e32 v61, 0, v61, vcc
	v_cndmask_b32_e64 v97, v61, v60, s[4:5]
	v_cvt_f16_f32_e32 v60, v48
	v_cvt_f32_f16_e32 v61, v60
	v_sub_f32_e32 v61, v48, v61
	v_cvt_f16_f32_e32 v61, v61
	v_cndmask_b32_e32 v61, 0, v61, vcc
	v_cndmask_b32_e64 v98, v61, v60, s[4:5]
	v_cvt_f16_f32_e32 v60, v49
	v_cvt_f32_f16_e32 v61, v60
	v_sub_f32_e32 v61, v49, v61
	v_cvt_f16_f32_e32 v61, v61
	v_cndmask_b32_e32 v61, 0, v61, vcc
	v_cndmask_b32_e64 v99, v61, v60, s[4:5]
	v_cvt_f16_f32_e32 v60, v50
	v_cvt_f32_f16_e32 v61, v60
	v_sub_f32_e32 v61, v50, v61
	v_cvt_f16_f32_e32 v61, v61
	v_cndmask_b32_e32 v61, 0, v61, vcc
	v_cndmask_b32_e64 v100, v61, v60, s[4:5]
	v_cvt_f16_f32_e32 v60, v51
	v_cvt_f32_f16_e32 v61, v60
	v_sub_f32_e32 v61, v51, v61
	v_cvt_f16_f32_e32 v61, v61
	v_cndmask_b32_e32 v61, 0, v61, vcc
	v_cndmask_b32_e64 v101, v61, v60, s[4:5]
	v_cvt_f16_f32_e32 v60, v52
	v_cvt_f32_f16_e32 v61, v60
	v_sub_f32_e32 v61, v52, v61
	v_cvt_f16_f32_e32 v61, v61
	v_cndmask_b32_e32 v61, 0, v61, vcc
	v_cndmask_b32_e64 v102, v61, v60, s[4:5]
	v_cvt_f16_f32_e32 v60, v53
	v_cvt_f32_f16_e32 v61, v60
	v_sub_f32_e32 v61, v53, v61
	v_cvt_f16_f32_e32 v61, v61
	v_cndmask_b32_e32 v61, 0, v61, vcc
	v_cndmask_b32_e64 v103, v61, v60, s[4:5]
	v_cvt_f16_f32_e32 v60, v54
	v_cvt_f32_f16_e32 v61, v60
	v_sub_f32_e32 v61, v54, v61
	v_cvt_f16_f32_e32 v61, v61
	v_cndmask_b32_e32 v61, 0, v61, vcc
	v_cndmask_b32_e64 v104, v61, v60, s[4:5]
	v_cvt_f16_f32_e32 v60, v55
	v_cvt_f32_f16_e32 v61, v60
	v_sub_f32_e32 v61, v55, v61
	v_cvt_f16_f32_e32 v61, v61
	v_cndmask_b32_e32 v61, 0, v61, vcc
	v_cndmask_b32_e64 v105, v61, v60, s[4:5]
	v_cvt_f16_f32_e32 v60, v56
	v_cvt_f32_f16_e32 v61, v60
	v_sub_f32_e32 v61, v56, v61
	v_cvt_f16_f32_e32 v61, v61
	v_cndmask_b32_e32 v61, 0, v61, vcc
	v_cndmask_b32_e64 v106, v61, v60, s[4:5]
	v_cvt_f16_f32_e32 v60, v57
	v_cvt_f32_f16_e32 v61, v60
	v_sub_f32_e32 v61, v57, v61
	v_cvt_f16_f32_e32 v61, v61
	v_cndmask_b32_e32 v61, 0, v61, vcc
	v_cndmask_b32_e64 v107, v61, v60, s[4:5]
	v_cvt_f16_f32_e32 v60, v58
	v_cvt_f32_f16_e32 v61, v60
	v_sub_f32_e32 v61, v58, v61
	v_cvt_f16_f32_e32 v61, v61
	v_cndmask_b32_e32 v61, 0, v61, vcc
	v_cndmask_b32_e64 v108, v61, v60, s[4:5]
	v_cvt_f16_f32_e32 v60, v59
	v_cvt_f32_f16_e32 v61, v60
	v_sub_f32_e32 v61, v59, v61
	v_cvt_f16_f32_e32 v61, v61
	v_cndmask_b32_e32 v61, 0, v61, vcc
	v_cndmask_b32_e64 v109, v61, v60, s[4:5]
	v_pack_b32_f16 v116, v94, v95
	v_pack_b32_f16 v117, v96, v97
	v_pack_b32_f16 v118, v98, v99
	v_pack_b32_f16 v119, v100, v101
	v_pack_b32_f16 v120, v102, v103
	v_pack_b32_f16 v121, v104, v105
	v_pack_b32_f16 v122, v106, v107
	v_pack_b32_f16 v123, v108, v109
	s_barrier
	ds_read_b128 v[44:47], v75 offset:0
	ds_read_b128 v[68:71], v75 offset:1024
	s_waitcnt lgkmcnt(0)
	v_mfma_f32_16x16x32_f16 v[84:87], v[2:5], v[44:47], v[18:21]
	v_mfma_f32_16x16x32_f16 v[88:91], v[14:17], v[44:47], v[38:41]
	v_mfma_f32_16x16x32_f16 v[84:87], v[6:9], v[68:71], v[84:87]
	v_mfma_f32_16x16x32_f16 v[88:91], v[10:13], v[68:71], v[88:91]
	s_barrier
	ds_read_b128 v[56:59], v75 offset:6144
	ds_read_b128 v[60:63], v75 offset:7168
	ds_read_b128 v[44:47], v75 offset:2048
	ds_read_b128 v[68:71], v75 offset:3072
	s_waitcnt lgkmcnt(3)
	v_mfma_f32_16x16x32_f16 v[84:87], v[30:33], v[56:59], v[84:87]
	v_mfma_f32_16x16x32_f16 v[88:91], v[22:25], v[56:59], v[88:91]
	s_waitcnt lgkmcnt(2)
	v_mfma_f32_16x16x32_f16 v[84:87], v[34:37], v[60:63], v[84:87]
	v_mfma_f32_16x16x32_f16 v[88:91], v[26:29], v[60:63], v[88:91]
	s_nop 7
	v_exp_f32_e32 v94, v86
	v_exp_f32_e32 v95, v90
	v_exp_f32_e32 v96, v84
	v_exp_f32_e32 v97, v88
	v_exp_f32_e32 v98, v85
	v_exp_f32_e32 v99, v89
	v_pk_add_f32 v[100:101], v[94:95], 1.0 op_sel_hi:[1,0]
	v_pk_fma_f32 v[102:103], v[94:95], s[8:9], v[92:93] op_sel_hi:[1,0,0]
	v_pk_fma_f32 v[100:101], v[96:97], v[100:101], v[100:101]
	v_pk_fma_f32 v[104:105], v[100:101], v[98:99], v[100:101]
	v_rcp_f32_e32 v104, v104
	v_rcp_f32_e32 v105, v105
	v_pk_fma_f32 v[102:103], v[102:103], v[98:99], v[102:103]
	v_pk_fma_f32 v[102:103], v[64:65], v[100:101], v[102:103]
	v_exp_f32_e32 v106, v87
	v_pk_mul_f32 v[64:65], v[102:103], v[104:105]
	v_exp_f32_e32 v108, v64
	v_exp_f32_e32 v109, v65
	v_exp_f32_e32 v107, v91
	v_pk_add_f32 v[110:111], v[108:109], 1.0 op_sel_hi:[1,0]
	v_pk_fma_f32 v[110:111], v[110:111], v[106:107], v[110:111]
	v_rcp_f32_e32 v110, v110
	v_rcp_f32_e32 v111, v111
	v_pk_add_f32 v[112:113], v[108:109], -1.0 op_sel_hi:[1,0]
	v_pk_mul_f32 v[112:113], v[112:113], v[110:111]
	v_cvt_pk_f16_f32 v114, v112, v113
	ds_write_b32 v81, v114 offset:4096
	s_waitcnt lgkmcnt(1)
	v_mfma_f32_16x16x32_f16 v[84:87], v[2:5], v[44:47], v[18:21]
	v_mfma_f32_16x16x32_f16 v[88:91], v[14:17], v[44:47], v[38:41]
	v_mfma_f32_16x16x32_f16 v[84:87], v[6:9], v[68:71], v[84:87]
	v_mfma_f32_16x16x32_f16 v[88:91], v[10:13], v[68:71], v[88:91]
	s_waitcnt lgkmcnt(0)
	s_barrier
	ds_read_b128 v[56:59], v75 offset:4096
	ds_read_b128 v[60:63], v75 offset:5120
	ds_read_b128 v[44:47], v75 offset:0
	ds_read_b128 v[68:71], v75 offset:1024
	s_waitcnt lgkmcnt(3)
	v_mfma_f32_16x16x32_f16 v[84:87], v[30:33], v[56:59], v[84:87]
	v_mfma_f32_16x16x32_f16 v[88:91], v[22:25], v[56:59], v[88:91]
	s_waitcnt lgkmcnt(2)
	v_mfma_f32_16x16x32_f16 v[84:87], v[34:37], v[60:63], v[84:87]
	v_mfma_f32_16x16x32_f16 v[88:91], v[26:29], v[60:63], v[88:91]
	s_cmp_eq_u32 s34, 0
	s_cbranch_scc0 .Lcb_o1_1
	v_mfma_f32_16x16x32_f16 v[50:53], v[116:119], v[56:59], 0
	s_nop 7
	v_add_f32_e32 v125, v50, v51
	s_mov_b64 s[16:17], exec
	s_mov_b64 exec, s[30:31]
	ds_write_b32 v74, v125 offset:128
	s_mov_b64 exec, s[16:17]
	s_branch .Lcb_o1s_3
.Lcb_o1_1:
	s_cmp_eq_u32 s34, 1
	s_cbranch_scc0 .Lcb_o1s_3
	v_mfma_f32_16x16x32_f16 v[50:53], v[120:123], v[60:63], 0
	s_nop 7
	v_add_f32_e32 v125, v50, v51
	s_mov_b64 s[16:17], exec
	s_mov_b64 exec, s[30:31]
	ds_write_b32 v74, v125 offset:192
	s_mov_b64 exec, s[16:17]
.Lcb_o1s_3:
	s_nop 7
	v_exp_f32_e32 v94, v86
	v_exp_f32_e32 v95, v90
	v_exp_f32_e32 v96, v84
	v_exp_f32_e32 v97, v88
	v_exp_f32_e32 v98, v85
	v_exp_f32_e32 v99, v89
	v_pk_add_f32 v[100:101], v[94:95], 1.0 op_sel_hi:[1,0]
	v_pk_fma_f32 v[102:103], v[94:95], s[8:9], v[92:93] op_sel_hi:[1,0,0]
	v_pk_fma_f32 v[100:101], v[96:97], v[100:101], v[100:101]
	v_pk_fma_f32 v[104:105], v[100:101], v[98:99], v[100:101]
	v_rcp_f32_e32 v104, v104
	v_rcp_f32_e32 v105, v105
	v_pk_fma_f32 v[102:103], v[102:103], v[98:99], v[102:103]
	v_pk_fma_f32 v[102:103], v[64:65], v[100:101], v[102:103]
	v_exp_f32_e32 v106, v87
	v_pk_mul_f32 v[64:65], v[102:103], v[104:105]
	v_exp_f32_e32 v108, v64
	v_exp_f32_e32 v109, v65
	v_exp_f32_e32 v107, v91
	v_pk_add_f32 v[110:111], v[108:109], 1.0 op_sel_hi:[1,0]
	v_pk_fma_f32 v[110:111], v[110:111], v[106:107], v[110:111]
	v_rcp_f32_e32 v110, v110
	v_rcp_f32_e32 v111, v111
	v_pk_add_f32 v[112:113], v[108:109], -1.0 op_sel_hi:[1,0]
	v_pk_mul_f32 v[112:113], v[112:113], v[110:111]
	v_cvt_pk_f16_f32 v114, v112, v113
	ds_write_b32 v81, v114 offset:6144
	s_waitcnt lgkmcnt(1)
	v_mfma_f32_16x16x32_f16 v[84:87], v[2:5], v[44:47], v[18:21]
	v_mfma_f32_16x16x32_f16 v[88:91], v[14:17], v[44:47], v[38:41]
	v_mfma_f32_16x16x32_f16 v[84:87], v[6:9], v[68:71], v[84:87]
	v_mfma_f32_16x16x32_f16 v[88:91], v[10:13], v[68:71], v[88:91]
	s_waitcnt lgkmcnt(0)
.Lcb_loop:
	s_barrier
	ds_read_b128 v[56:59], v75 offset:6144
	ds_read_b128 v[60:63], v75 offset:7168
	ds_read_b128 v[44:47], v75 offset:2048
	ds_read_b128 v[68:71], v75 offset:3072
	s_waitcnt lgkmcnt(3)
	v_mfma_f32_16x16x32_f16 v[84:87], v[30:33], v[56:59], v[84:87]
	v_mfma_f32_16x16x32_f16 v[88:91], v[22:25], v[56:59], v[88:91]
	s_waitcnt lgkmcnt(2)
	v_mfma_f32_16x16x32_f16 v[84:87], v[34:37], v[60:63], v[84:87]
	v_mfma_f32_16x16x32_f16 v[88:91], v[26:29], v[60:63], v[88:91]
	s_cmp_eq_u32 s34, 0
	s_cbranch_scc0 .Lcb_o1_4
	v_mfma_f32_16x16x32_f16 v[50:53], v[116:119], v[56:59], 0
	s_nop 7
	v_add_f32_e32 v125, v50, v51
	s_mov_b64 s[16:17], exec
	s_mov_b64 exec, s[30:31]
	ds_write_b32 v74, v125 offset:0
	s_mov_b64 exec, s[16:17]
	s_branch .Lcb_o1s_6
.Lcb_o1_4:
	s_cmp_eq_u32 s34, 1
	s_cbranch_scc0 .Lcb_o1s_6
	v_mfma_f32_16x16x32_f16 v[50:53], v[120:123], v[60:63], 0
	s_nop 7
	v_add_f32_e32 v125, v50, v51
	s_mov_b64 s[16:17], exec
	s_mov_b64 exec, s[30:31]
	ds_write_b32 v74, v125 offset:64
	s_mov_b64 exec, s[16:17]
.Lcb_o1s_6:
	s_cmp_eq_u32 s34, 2
	s_cbranch_scc0 .Lcb_o2s_7
	ds_read_b32 v125, v74 offset:128
	ds_read_b32 v126, v74 offset:192
	s_waitcnt lgkmcnt(0)
	v_add_f32_e32 v125, v125, v126
	v_add_f32_e32 v125, s28, v125
	v_mul_f32_e32 v126, 0x3fb8aa3b, v125
	v_exp_f32_e32 v126, v126
	v_cmp_lt_f32_e32 vcc, 0, v125
	v_add_f32_e32 v126, -1.0, v126
	v_mul_f32_e32 v126, 0x3fe10966, v126
	v_mul_f32_e32 v125, 0x3f867d5f, v125
	s_nop 0
	v_cndmask_b32_e32 v125, v126, v125, vcc
	s_mov_b64 s[16:17], exec
	s_mov_b64 exec, s[30:31]
	global_store_dword v124, v125, s[26:27] offset:0
	s_mov_b64 exec, s[16:17]
.Lcb_o2s_7:
	s_nop 7
	v_exp_f32_e32 v94, v86
	v_exp_f32_e32 v95, v90
	v_exp_f32_e32 v96, v84
	v_exp_f32_e32 v97, v88
	v_exp_f32_e32 v98, v85
	v_exp_f32_e32 v99, v89
	v_pk_add_f32 v[100:101], v[94:95], 1.0 op_sel_hi:[1,0]
	v_pk_fma_f32 v[102:103], v[94:95], s[8:9], v[92:93] op_sel_hi:[1,0,0]
	v_pk_fma_f32 v[100:101], v[96:97], v[100:101], v[100:101]
	v_pk_fma_f32 v[104:105], v[100:101], v[98:99], v[100:101]
	v_rcp_f32_e32 v104, v104
	v_rcp_f32_e32 v105, v105
	v_pk_fma_f32 v[102:103], v[102:103], v[98:99], v[102:103]
	v_pk_fma_f32 v[102:103], v[64:65], v[100:101], v[102:103]
	v_exp_f32_e32 v106, v87
	v_pk_mul_f32 v[64:65], v[102:103], v[104:105]
	v_exp_f32_e32 v108, v64
	v_exp_f32_e32 v109, v65
	v_exp_f32_e32 v107, v91
	v_pk_add_f32 v[110:111], v[108:109], 1.0 op_sel_hi:[1,0]
	v_pk_fma_f32 v[110:111], v[110:111], v[106:107], v[110:111]
	v_rcp_f32_e32 v110, v110
	v_rcp_f32_e32 v111, v111
	v_pk_add_f32 v[112:113], v[108:109], -1.0 op_sel_hi:[1,0]
	v_pk_mul_f32 v[112:113], v[112:113], v[110:111]
	v_cvt_pk_f16_f32 v114, v112, v113
	ds_write_b32 v81, v114 offset:4096
	s_waitcnt lgkmcnt(1)
	v_mfma_f32_16x16x32_f16 v[84:87], v[2:5], v[44:47], v[18:21]
	v_mfma_f32_16x16x32_f16 v[88:91], v[14:17], v[44:47], v[38:41]
	v_mfma_f32_16x16x32_f16 v[84:87], v[6:9], v[68:71], v[84:87]
	v_mfma_f32_16x16x32_f16 v[88:91], v[10:13], v[68:71], v[88:91]
	s_waitcnt lgkmcnt(0)
	s_barrier
	ds_read_b128 v[56:59], v75 offset:4096
	ds_read_b128 v[60:63], v75 offset:5120
	ds_read_b128 v[44:47], v75 offset:0
	ds_read_b128 v[68:71], v75 offset:1024
	s_waitcnt lgkmcnt(3)
	v_mfma_f32_16x16x32_f16 v[84:87], v[30:33], v[56:59], v[84:87]
	v_mfma_f32_16x16x32_f16 v[88:91], v[22:25], v[56:59], v[88:91]
	s_waitcnt lgkmcnt(2)
	v_mfma_f32_16x16x32_f16 v[84:87], v[34:37], v[60:63], v[84:87]
	v_mfma_f32_16x16x32_f16 v[88:91], v[26:29], v[60:63], v[88:91]
	s_cmp_eq_u32 s34, 0
	s_cbranch_scc0 .Lcb_o1_8
	v_mfma_f32_16x16x32_f16 v[50:53], v[116:119], v[56:59], 0
	s_nop 7
	v_add_f32_e32 v125, v50, v51
	s_mov_b64 s[16:17], exec
	s_mov_b64 exec, s[30:31]
	ds_write_b32 v74, v125 offset:128
	s_mov_b64 exec, s[16:17]
	s_branch .Lcb_o1s_10

.Lcb_o1s_10:
	s_cmp_eq_u32 s34, 2
	s_cbranch_scc0 .Lcb_o2s_11
	ds_read_b32 v125, v74 offset:0
	ds_read_b32 v126, v74 offset:64
	s_waitcnt lgkmcnt(0)
	v_add_f32_e32 v125, v125, v126
	v_add_f32_e32 v125, s28, v125
	v_mul_f32_e32 v126, 0x3fb8aa3b, v125
	v_exp_f32_e32 v126, v126
	v_cmp_lt_f32_e32 vcc, 0, v125
	v_add_f32_e32 v126, -1.0, v126
	v_mul_f32_e32 v126, 0x3fe10966, v126
	v_mul_f32_e32 v125, 0x3f867d5f, v125
	s_nop 0
	v_cndmask_b32_e32 v125, v126, v125, vcc
	s_mov_b64 s[16:17], exec
	s_mov_b64 exec, s[30:31]
	global_store_dword v124, v125, s[26:27] offset:4
	s_mov_b64 exec, s[16:17]
.Lcb_o2s_11:
	s_nop 7
	v_exp_f32_e32 v94, v86
	v_exp_f32_e32 v95, v90
	v_exp_f32_e32 v96, v84
	v_exp_f32_e32 v97, v88
	v_exp_f32_e32 v98, v85
	v_exp_f32_e32 v99, v89
	v_pk_add_f32 v[100:101], v[94:95], 1.0 op_sel_hi:[1,0]
	v_pk_fma_f32 v[102:103], v[94:95], s[8:9], v[92:93] op_sel_hi:[1,0,0]
	v_pk_fma_f32 v[100:101], v[96:97], v[100:101], v[100:101]
	v_pk_fma_f32 v[104:105], v[100:101], v[98:99], v[100:101]
	v_rcp_f32_e32 v104, v104
	v_rcp_f32_e32 v105, v105
	v_pk_fma_f32 v[102:103], v[102:103], v[98:99], v[102:103]
	v_pk_fma_f32 v[102:103], v[64:65], v[100:101], v[102:103]
	v_exp_f32_e32 v106, v87
	v_pk_mul_f32 v[64:65], v[102:103], v[104:105]
	v_exp_f32_e32 v108, v64
	v_exp_f32_e32 v109, v65
	v_exp_f32_e32 v107, v91
	v_pk_add_f32 v[110:111], v[108:109], 1.0 op_sel_hi:[1,0]
	v_pk_fma_f32 v[110:111], v[110:111], v[106:107], v[110:111]
	v_rcp_f32_e32 v110, v110
	v_rcp_f32_e32 v111, v111
	v_pk_add_f32 v[112:113], v[108:109], -1.0 op_sel_hi:[1,0]
	v_pk_mul_f32 v[112:113], v[112:113], v[110:111]
	v_cvt_pk_f16_f32 v114, v112, v113
	ds_write_b32 v81, v114 offset:6144
	s_waitcnt lgkmcnt(1)
	v_mfma_f32_16x16x32_f16 v[84:87], v[2:5], v[44:47], v[18:21]
	v_mfma_f32_16x16x32_f16 v[88:91], v[14:17], v[44:47], v[38:41]
	v_mfma_f32_16x16x32_f16 v[84:87], v[6:9], v[68:71], v[84:87]
	v_mfma_f32_16x16x32_f16 v[88:91], v[10:13], v[68:71], v[88:91]
	s_waitcnt lgkmcnt(0)
	s_barrier
	ds_read_b128 v[56:59], v75 offset:6144
	ds_read_b128 v[60:63], v75 offset:7168
	ds_read_b128 v[44:47], v75 offset:2048
	ds_read_b128 v[68:71], v75 offset:3072
	s_waitcnt lgkmcnt(3)
	v_mfma_f32_16x16x32_f16 v[84:87], v[30:33], v[56:59], v[84:87]
	v_mfma_f32_16x16x32_f16 v[88:91], v[22:25], v[56:59], v[88:91]
	s_waitcnt lgkmcnt(2)
	v_mfma_f32_16x16x32_f16 v[84:87], v[34:37], v[60:63], v[84:87]
	v_mfma_f32_16x16x32_f16 v[88:91], v[26:29], v[60:63], v[88:91]
	s_cmp_eq_u32 s34, 0
	s_cbranch_scc0 .Lcb_o1_12
	v_mfma_f32_16x16x32_f16 v[50:53], v[116:119], v[56:59], 0
	s_nop 7
	v_add_f32_e32 v125, v50, v51
	s_mov_b64 s[16:17], exec
	s_mov_b64 exec, s[30:31]
	ds_write_b32 v74, v125 offset:0
	s_mov_b64 exec, s[16:17]
	s_branch .Lcb_o1s_14

.Lcb_o1s_14:
	s_cmp_eq_u32 s34, 2
	s_cbranch_scc0 .Lcb_o2s_15
	ds_read_b32 v125, v74 offset:128
	ds_read_b32 v126, v74 offset:192
	s_waitcnt lgkmcnt(0)
	v_add_f32_e32 v125, v125, v126
	v_add_f32_e32 v125, s28, v125
	v_mul_f32_e32 v126, 0x3fb8aa3b, v125
	v_exp_f32_e32 v126, v126
	v_cmp_lt_f32_e32 vcc, 0, v125
	v_add_f32_e32 v126, -1.0, v126
	v_mul_f32_e32 v126, 0x3fe10966, v126
	v_mul_f32_e32 v125, 0x3f867d5f, v125
	s_nop 0
	v_cndmask_b32_e32 v125, v126, v125, vcc
	s_mov_b64 s[16:17], exec
	s_mov_b64 exec, s[30:31]
	global_store_dword v124, v125, s[26:27] offset:8
	s_mov_b64 exec, s[16:17]

.Lcb_o1s_18:
	s_cmp_eq_u32 s34, 2
	s_cbranch_scc0 .Lcb_o2s_19
	ds_read_b32 v125, v74 offset:0
	ds_read_b32 v126, v74 offset:64
	s_waitcnt lgkmcnt(0)
	v_add_f32_e32 v125, v125, v126
	v_add_f32_e32 v125, s28, v125
	v_mul_f32_e32 v126, 0x3fb8aa3b, v125
	v_exp_f32_e32 v126, v126
	v_cmp_lt_f32_e32 vcc, 0, v125
	v_add_f32_e32 v126, -1.0, v126
	v_mul_f32_e32 v126, 0x3fe10966, v126
	v_mul_f32_e32 v125, 0x3f867d5f, v125
	s_nop 0
	v_cndmask_b32_e32 v125, v126, v125, vcc
	s_mov_b64 s[16:17], exec
	s_mov_b64 exec, s[30:31]
	global_store_dword v124, v125, s[26:27] offset:12
	s_mov_b64 exec, s[16:17]
.Lcb_o2s_19:
	s_nop 7
	v_exp_f32_e32 v94, v86
	v_exp_f32_e32 v95, v90
	v_exp_f32_e32 v96, v84
	v_exp_f32_e32 v97, v88
	v_exp_f32_e32 v98, v85
	v_exp_f32_e32 v99, v89
	v_pk_add_f32 v[100:101], v[94:95], 1.0 op_sel_hi:[1,0]
	v_pk_fma_f32 v[102:103], v[94:95], s[8:9], v[92:93] op_sel_hi:[1,0,0]
	v_pk_fma_f32 v[100:101], v[96:97], v[100:101], v[100:101]
	v_pk_fma_f32 v[104:105], v[100:101], v[98:99], v[100:101]
	v_rcp_f32_e32 v104, v104
	v_rcp_f32_e32 v105, v105
	v_pk_fma_f32 v[102:103], v[102:103], v[98:99], v[102:103]
	v_pk_fma_f32 v[102:103], v[64:65], v[100:101], v[102:103]
	v_exp_f32_e32 v106, v87
	v_pk_mul_f32 v[64:65], v[102:103], v[104:105]
	v_exp_f32_e32 v108, v64
	v_exp_f32_e32 v109, v65
	v_exp_f32_e32 v107, v91
	v_pk_add_f32 v[110:111], v[108:109], 1.0 op_sel_hi:[1,0]
	v_pk_fma_f32 v[110:111], v[110:111], v[106:107], v[110:111]
	v_rcp_f32_e32 v110, v110
	v_rcp_f32_e32 v111, v111
	v_pk_add_f32 v[112:113], v[108:109], -1.0 op_sel_hi:[1,0]
	v_pk_mul_f32 v[112:113], v[112:113], v[110:111]
	v_cvt_pk_f16_f32 v114, v112, v113
	ds_write_b32 v81, v114 offset:6144
	s_waitcnt lgkmcnt(1)
	v_mfma_f32_16x16x32_f16 v[84:87], v[2:5], v[44:47], v[18:21]
	v_mfma_f32_16x16x32_f16 v[88:91], v[14:17], v[44:47], v[38:41]
	v_mfma_f32_16x16x32_f16 v[84:87], v[6:9], v[68:71], v[84:87]
	v_mfma_f32_16x16x32_f16 v[88:91], v[10:13], v[68:71], v[88:91]
	s_waitcnt lgkmcnt(0)
	v_min_f32_e32 v64, 0x42700000, v64
	v_min_f32_e32 v65, 0x42700000, v65
	s_add_u32 s12, s12, 4
	v_add_u32_e32 v124, 16, v124
	s_cmp_lt_u32 s12, 452
	s_cbranch_scc1 .Lcb_loop
	s_barrier
	ds_read_b128 v[56:59], v75 offset:6144
	ds_read_b128 v[60:63], v75 offset:7168
	s_waitcnt lgkmcnt(0)
	s_cmp_eq_u32 s34, 0
	s_cbranch_scc0 .Lcb_o1_20
	v_mfma_f32_16x16x32_f16 v[50:53], v[116:119], v[56:59], 0
	s_nop 7
	v_add_f32_e32 v125, v50, v51
	s_mov_b64 s[16:17], exec
	s_mov_b64 exec, s[30:31]
	ds_write_b32 v74, v125 offset:0
	s_mov_b64 exec, s[16:17]
	s_branch .Lcb_o1s_22

.Lcb_o2s_23:
	s_waitcnt lgkmcnt(0)
	s_barrier
	s_cmp_eq_u32 s34, 2
	s_cbranch_scc0 .Lcb_o2s_24
	ds_read_b32 v125, v74 offset:0
	ds_read_b32 v126, v74 offset:64
	s_waitcnt lgkmcnt(0)
	v_add_f32_e32 v125, v125, v126
	v_add_f32_e32 v125, s28, v125
	v_mul_f32_e32 v126, 0x3fb8aa3b, v125
	v_exp_f32_e32 v126, v126
	v_cmp_lt_f32_e32 vcc, 0, v125
	v_add_f32_e32 v126, -1.0, v126
	v_mul_f32_e32 v126, 0x3fe10966, v126
	v_mul_f32_e32 v125, 0x3f867d5f, v125
	s_nop 0
	v_cndmask_b32_e32 v125, v126, v125, vcc
	s_mov_b64 s[16:17], exec
	s_mov_b64 exec, s[30:31]
	global_store_dword v124, v125, s[26:27] offset:4
	s_mov_b64 exec, s[16:17]
.Lcb_o2s_24:
	s_waitcnt lgkmcnt(0)
	s_endpgm

.Lk_144:
	v_or_b32_e32 v46, 0x400, v54
	buffer_load_dwordx4 v[46:49], v46, s[4:7], 0 offen sc1
	ds_read_b128 v[50:53], v1
	v_mov_b32_e32 v66, 0
	v_add_u32_e32 v63, 0x800, v54
	s_mov_b32 s9, 0
	v_mov_b32_e32 v67, 0
	v_mov_b32_e32 v68, 0
	v_mov_b32_e32 v62, 0xc038aa3b
	s_mov_b32 s8, 0x4038aa3b
	v_mov_b32_e32 v65, 0
	v_mov_b32_e32 v64, v66
	s_setprio 2
	v_mov_b32_e32 v92, 0xc038aa3b
	v_mov_b32_e32 v93, 0xc038aa3b
	s_mov_b32 s8, 0x4038aa3b
	s_mov_b32 s9, 0
	v_mov_b32_e32 v64, 0
	v_mov_b32_e32 v65, 0
	v_mov_b32_e32 v66, 0
	v_mov_b32_e32 v67, 0
	v_mov_b32_e32 v68, 0
	v_mov_b32_e32 v116, v1
	v_mov_b32_e32 v117, v63
	s_mov_b32 s12, 0
	s_waitcnt lgkmcnt(0)
	s_waitcnt vmcnt(1)
	v_mfma_f32_16x16x32_f16 v[84:87], v[2:5], v[42:45], v[18:21]
	v_mfma_f32_16x16x32_f16 v[88:91], v[14:17], v[42:45], v[38:41]
	ds_read_b128 v[56:59], v75 offset:2048
	ds_read_b128 v[60:63], v75 offset:3072
	v_mfma_f32_16x16x32_f16 v[84:87], v[6:9], v[50:53], v[84:87]
	v_mfma_f32_16x16x32_f16 v[88:91], v[10:13], v[50:53], v[88:91]
	v_readfirstlane_b32 s10, v67
	v_readfirstlane_b32 s11, v68
	global_load_dword v67, v66, s[0:1] sc1
	global_load_dword v68, v66, s[0:1] offset:4 sc1
	s_min_u32 s10, s10, s11
	s_max_u32 s14, s14, s10
	s_waitcnt lgkmcnt(1)
	v_mfma_f32_16x16x32_f16 v[84:87], v[30:33], v[56:59], v[84:87]
	v_mfma_f32_16x16x32_f16 v[88:91], v[22:25], v[56:59], v[88:91]
	s_waitcnt lgkmcnt(0)
	v_mfma_f32_16x16x32_f16 v[84:87], v[34:37], v[60:63], v[84:87]
	v_mfma_f32_16x16x32_f16 v[88:91], v[26:29], v[60:63], v[88:91]
	s_add_u32 s13, s12, 3
	s_min_u32 s13, s13, 450
	s_cmp_ge_u32 s14, s13
	s_cbranch_scc1 .Lca_ok_1
	s_mov_b32 s15, 0

.Lca_ok_1:
	buffer_load_dwordx4 v[42:45], v117, s[4:7], 0 offen offset:0 sc1
	ds_read_b128 v[50:53], v116 offset:256
	s_nop 1
	v_exp_f32_e32 v94, v86
	v_exp_f32_e32 v95, v90
	v_exp_f32_e32 v96, v84
	v_exp_f32_e32 v97, v88
	v_exp_f32_e32 v98, v85
	v_exp_f32_e32 v99, v89
	v_pk_add_f32 v[100:101], v[94:95], 1.0 op_sel_hi:[1,0]
	v_pk_fma_f32 v[102:103], v[94:95], s[8:9], v[92:93] op_sel_hi:[1,0,0]
	v_pk_fma_f32 v[100:101], v[96:97], v[100:101], v[100:101]
	v_pk_fma_f32 v[104:105], v[100:101], v[98:99], v[100:101]
	v_rcp_f32_e32 v104, v104
	v_rcp_f32_e32 v105, v105
	v_pk_fma_f32 v[102:103], v[102:103], v[98:99], v[102:103]
	v_pk_fma_f32 v[102:103], v[64:65], v[100:101], v[102:103]
	v_exp_f32_e32 v106, v87
	v_pk_mul_f32 v[64:65], v[102:103], v[104:105]
	v_exp_f32_e32 v108, v64
	v_exp_f32_e32 v109, v65
	v_exp_f32_e32 v107, v91
	v_pk_add_f32 v[110:111], v[108:109], 1.0 op_sel_hi:[1,0]
	v_pk_fma_f32 v[110:111], v[110:111], v[106:107], v[110:111]
	v_rcp_f32_e32 v110, v110
	v_rcp_f32_e32 v111, v111
	v_pk_add_f32 v[112:113], v[108:109], -1.0 op_sel_hi:[1,0]
	v_pk_mul_f32 v[112:113], v[112:113], v[110:111]
	v_cvt_pk_f16_f32 v114, v112, v113
	ds_write_b32 v81, v114 offset:0
	s_waitcnt lgkmcnt(0)
	s_barrier
	s_waitcnt vmcnt(3)
	v_mfma_f32_16x16x32_f16 v[84:87], v[2:5], v[46:49], v[18:21]
	v_mfma_f32_16x16x32_f16 v[88:91], v[14:17], v[46:49], v[38:41]
	ds_read_b128 v[56:59], v75 offset:0
	ds_read_b128 v[60:63], v75 offset:1024
	v_mfma_f32_16x16x32_f16 v[84:87], v[6:9], v[50:53], v[84:87]
	v_mfma_f32_16x16x32_f16 v[88:91], v[10:13], v[50:53], v[88:91]
	s_waitcnt lgkmcnt(1)
	v_mfma_f32_16x16x32_f16 v[84:87], v[30:33], v[56:59], v[84:87]
	v_mfma_f32_16x16x32_f16 v[88:91], v[22:25], v[56:59], v[88:91]
	s_waitcnt lgkmcnt(0)
	v_mfma_f32_16x16x32_f16 v[84:87], v[34:37], v[60:63], v[84:87]
	v_mfma_f32_16x16x32_f16 v[88:91], v[26:29], v[60:63], v[88:91]
	s_add_u32 s13, s12, 4
	s_min_u32 s13, s13, 450
	s_cmp_ge_u32 s14, s13
	s_cbranch_scc1 .Lca_ok_3
	s_mov_b32 s15, 0

.Lca_ok_3:
	buffer_load_dwordx4 v[46:49], v117, s[4:7], 0 offen offset:1024 sc1
	ds_read_b128 v[50:53], v116 offset:512
	s_nop 1
	v_exp_f32_e32 v94, v86
	v_exp_f32_e32 v95, v90
	v_exp_f32_e32 v96, v84
	v_exp_f32_e32 v97, v88
	v_exp_f32_e32 v98, v85
	v_exp_f32_e32 v99, v89
	v_pk_add_f32 v[100:101], v[94:95], 1.0 op_sel_hi:[1,0]
	v_pk_fma_f32 v[102:103], v[94:95], s[8:9], v[92:93] op_sel_hi:[1,0,0]
	v_pk_fma_f32 v[100:101], v[96:97], v[100:101], v[100:101]
	v_pk_fma_f32 v[104:105], v[100:101], v[98:99], v[100:101]
	v_rcp_f32_e32 v104, v104
	v_rcp_f32_e32 v105, v105
	v_pk_fma_f32 v[102:103], v[102:103], v[98:99], v[102:103]
	v_pk_fma_f32 v[102:103], v[64:65], v[100:101], v[102:103]
	v_exp_f32_e32 v106, v87
	v_pk_mul_f32 v[64:65], v[102:103], v[104:105]
	v_exp_f32_e32 v108, v64
	v_exp_f32_e32 v109, v65
	v_exp_f32_e32 v107, v91
	v_pk_add_f32 v[110:111], v[108:109], 1.0 op_sel_hi:[1,0]
	v_pk_fma_f32 v[110:111], v[110:111], v[106:107], v[110:111]
	v_rcp_f32_e32 v110, v110
	v_rcp_f32_e32 v111, v111
	v_pk_add_f32 v[112:113], v[108:109], -1.0 op_sel_hi:[1,0]
	v_pk_mul_f32 v[112:113], v[112:113], v[110:111]
	v_cvt_pk_f16_f32 v114, v112, v113
	ds_write_b32 v81, v114 offset:2048
	s_waitcnt lgkmcnt(0)
	v_add_u32_e32 v116, 0x200, v116
	v_add_u32_e32 v117, 0x800, v117
	s_mov_b32 s12, 2
.Lca_loop:
	s_barrier
	s_waitcnt vmcnt(1)
	v_mfma_f32_16x16x32_f16 v[84:87], v[2:5], v[42:45], v[18:21]
	v_mfma_f32_16x16x32_f16 v[88:91], v[14:17], v[42:45], v[38:41]
	ds_read_b128 v[56:59], v75 offset:2048
	ds_read_b128 v[60:63], v75 offset:3072
	v_mfma_f32_16x16x32_f16 v[84:87], v[6:9], v[50:53], v[84:87]
	v_mfma_f32_16x16x32_f16 v[88:91], v[10:13], v[50:53], v[88:91]
	v_readfirstlane_b32 s10, v67
	v_readfirstlane_b32 s11, v68
	global_load_dword v67, v66, s[0:1] sc1
	global_load_dword v68, v66, s[0:1] offset:4 sc1
	s_min_u32 s10, s10, s11
	s_max_u32 s14, s14, s10
	s_waitcnt lgkmcnt(1)
	v_mfma_f32_16x16x32_f16 v[84:87], v[30:33], v[56:59], v[84:87]
	v_mfma_f32_16x16x32_f16 v[88:91], v[22:25], v[56:59], v[88:91]
	s_waitcnt lgkmcnt(0)
	v_mfma_f32_16x16x32_f16 v[84:87], v[34:37], v[60:63], v[84:87]
	v_mfma_f32_16x16x32_f16 v[88:91], v[26:29], v[60:63], v[88:91]
	s_add_u32 s13, s12, 3
	s_min_u32 s13, s13, 450
	s_cmp_ge_u32 s14, s13
	s_cbranch_scc1 .Lca_ok_5
	s_mov_b32 s15, 0

.Lca_ok_5:
	buffer_load_dwordx4 v[42:45], v117, s[4:7], 0 offen offset:0 sc1
	ds_read_b128 v[50:53], v116 offset:256
	s_nop 1
	v_min_f32_e32 v64, 0x42700000, v64
	v_min_f32_e32 v65, 0x42700000, v65
	v_exp_f32_e32 v94, v86
	v_exp_f32_e32 v95, v90
	v_exp_f32_e32 v96, v84
	v_exp_f32_e32 v97, v88
	v_exp_f32_e32 v98, v85
	v_exp_f32_e32 v99, v89
	v_pk_add_f32 v[100:101], v[94:95], 1.0 op_sel_hi:[1,0]
	v_pk_fma_f32 v[102:103], v[94:95], s[8:9], v[92:93] op_sel_hi:[1,0,0]
	v_pk_fma_f32 v[100:101], v[96:97], v[100:101], v[100:101]
	v_pk_fma_f32 v[104:105], v[100:101], v[98:99], v[100:101]
	v_rcp_f32_e32 v104, v104
	v_rcp_f32_e32 v105, v105
	v_pk_fma_f32 v[102:103], v[102:103], v[98:99], v[102:103]
	v_pk_fma_f32 v[102:103], v[64:65], v[100:101], v[102:103]
	v_exp_f32_e32 v106, v87
	v_pk_mul_f32 v[64:65], v[102:103], v[104:105]
	v_exp_f32_e32 v108, v64
	v_exp_f32_e32 v109, v65
	v_exp_f32_e32 v107, v91
	v_pk_add_f32 v[110:111], v[108:109], 1.0 op_sel_hi:[1,0]
	v_pk_fma_f32 v[110:111], v[110:111], v[106:107], v[110:111]
	v_rcp_f32_e32 v110, v110
	v_rcp_f32_e32 v111, v111
	v_pk_add_f32 v[112:113], v[108:109], -1.0 op_sel_hi:[1,0]
	v_pk_mul_f32 v[112:113], v[112:113], v[110:111]
	v_cvt_pk_f16_f32 v114, v112, v113
	ds_write_b32 v81, v114 offset:0
	s_waitcnt lgkmcnt(0)
	s_barrier
	s_waitcnt vmcnt(3)
	v_mfma_f32_16x16x32_f16 v[84:87], v[2:5], v[46:49], v[18:21]
	v_mfma_f32_16x16x32_f16 v[88:91], v[14:17], v[46:49], v[38:41]
	ds_read_b128 v[56:59], v75 offset:0
	ds_read_b128 v[60:63], v75 offset:1024
	v_mfma_f32_16x16x32_f16 v[84:87], v[6:9], v[50:53], v[84:87]
	v_mfma_f32_16x16x32_f16 v[88:91], v[10:13], v[50:53], v[88:91]
	s_waitcnt lgkmcnt(1)
	v_mfma_f32_16x16x32_f16 v[84:87], v[30:33], v[56:59], v[84:87]
	v_mfma_f32_16x16x32_f16 v[88:91], v[22:25], v[56:59], v[88:91]
	s_waitcnt lgkmcnt(0)
	v_mfma_f32_16x16x32_f16 v[84:87], v[34:37], v[60:63], v[84:87]
	v_mfma_f32_16x16x32_f16 v[88:91], v[26:29], v[60:63], v[88:91]
	s_add_u32 s13, s12, 4
	s_min_u32 s13, s13, 450
	s_cmp_ge_u32 s14, s13
	s_cbranch_scc1 .Lca_ok_7
	s_mov_b32 s15, 0

.Lca_ok_7:
	buffer_load_dwordx4 v[46:49], v117, s[4:7], 0 offen offset:1024 sc1
	ds_read_b128 v[50:53], v116 offset:512
	s_nop 1
	v_exp_f32_e32 v94, v86
	v_exp_f32_e32 v95, v90
	v_exp_f32_e32 v96, v84
	v_exp_f32_e32 v97, v88
	v_exp_f32_e32 v98, v85
	v_exp_f32_e32 v99, v89
	v_pk_add_f32 v[100:101], v[94:95], 1.0 op_sel_hi:[1,0]
	v_pk_fma_f32 v[102:103], v[94:95], s[8:9], v[92:93] op_sel_hi:[1,0,0]
	v_pk_fma_f32 v[100:101], v[96:97], v[100:101], v[100:101]
	v_pk_fma_f32 v[104:105], v[100:101], v[98:99], v[100:101]
	v_rcp_f32_e32 v104, v104
	v_rcp_f32_e32 v105, v105
	v_pk_fma_f32 v[102:103], v[102:103], v[98:99], v[102:103]
	v_pk_fma_f32 v[102:103], v[64:65], v[100:101], v[102:103]
	v_exp_f32_e32 v106, v87
	v_pk_mul_f32 v[64:65], v[102:103], v[104:105]
	v_exp_f32_e32 v108, v64
	v_exp_f32_e32 v109, v65
	v_exp_f32_e32 v107, v91
	v_pk_add_f32 v[110:111], v[108:109], 1.0 op_sel_hi:[1,0]
	v_pk_fma_f32 v[110:111], v[110:111], v[106:107], v[110:111]
	v_rcp_f32_e32 v110, v110
	v_rcp_f32_e32 v111, v111
	v_pk_add_f32 v[112:113], v[108:109], -1.0 op_sel_hi:[1,0]
	v_pk_mul_f32 v[112:113], v[112:113], v[110:111]
	v_cvt_pk_f16_f32 v114, v112, v113
	ds_write_b32 v81, v114 offset:2048
	s_waitcnt lgkmcnt(0)
	s_barrier
	s_waitcnt vmcnt(1)
	v_mfma_f32_16x16x32_f16 v[84:87], v[2:5], v[42:45], v[18:21]
	v_mfma_f32_16x16x32_f16 v[88:91], v[14:17], v[42:45], v[38:41]
	ds_read_b128 v[56:59], v75 offset:2048
	ds_read_b128 v[60:63], v75 offset:3072
	v_mfma_f32_16x16x32_f16 v[84:87], v[6:9], v[50:53], v[84:87]
	v_mfma_f32_16x16x32_f16 v[88:91], v[10:13], v[50:53], v[88:91]
	v_readfirstlane_b32 s10, v67
	v_readfirstlane_b32 s11, v68
	global_load_dword v67, v66, s[0:1] sc1
	global_load_dword v68, v66, s[0:1] offset:4 sc1
	s_min_u32 s10, s10, s11
	s_max_u32 s14, s14, s10
	s_waitcnt lgkmcnt(1)
	v_mfma_f32_16x16x32_f16 v[84:87], v[30:33], v[56:59], v[84:87]
	v_mfma_f32_16x16x32_f16 v[88:91], v[22:25], v[56:59], v[88:91]
	s_waitcnt lgkmcnt(0)
	v_mfma_f32_16x16x32_f16 v[84:87], v[34:37], v[60:63], v[84:87]
	v_mfma_f32_16x16x32_f16 v[88:91], v[26:29], v[60:63], v[88:91]
	s_add_u32 s13, s12, 5
	s_min_u32 s13, s13, 450
	s_cmp_ge_u32 s14, s13
	s_cbranch_scc1 .Lca_ok_9
	s_mov_b32 s15, 0

.Lca_ok_9:
	buffer_load_dwordx4 v[42:45], v117, s[4:7], 0 offen offset:2048 sc1
	ds_read_b128 v[50:53], v116 offset:768
	s_nop 1
	v_exp_f32_e32 v94, v86
	v_exp_f32_e32 v95, v90
	v_exp_f32_e32 v96, v84
	v_exp_f32_e32 v97, v88
	v_exp_f32_e32 v98, v85
	v_exp_f32_e32 v99, v89
	v_pk_add_f32 v[100:101], v[94:95], 1.0 op_sel_hi:[1,0]
	v_pk_fma_f32 v[102:103], v[94:95], s[8:9], v[92:93] op_sel_hi:[1,0,0]
	v_pk_fma_f32 v[100:101], v[96:97], v[100:101], v[100:101]
	v_pk_fma_f32 v[104:105], v[100:101], v[98:99], v[100:101]
	v_rcp_f32_e32 v104, v104
	v_rcp_f32_e32 v105, v105
	v_pk_fma_f32 v[102:103], v[102:103], v[98:99], v[102:103]
	v_pk_fma_f32 v[102:103], v[64:65], v[100:101], v[102:103]
	v_exp_f32_e32 v106, v87
	v_pk_mul_f32 v[64:65], v[102:103], v[104:105]
	v_exp_f32_e32 v108, v64
	v_exp_f32_e32 v109, v65
	v_exp_f32_e32 v107, v91
	v_pk_add_f32 v[110:111], v[108:109], 1.0 op_sel_hi:[1,0]
	v_pk_fma_f32 v[110:111], v[110:111], v[106:107], v[110:111]
	v_rcp_f32_e32 v110, v110
	v_rcp_f32_e32 v111, v111
	v_pk_add_f32 v[112:113], v[108:109], -1.0 op_sel_hi:[1,0]
	v_pk_mul_f32 v[112:113], v[112:113], v[110:111]
	v_cvt_pk_f16_f32 v114, v112, v113
	ds_write_b32 v81, v114 offset:0
	s_waitcnt lgkmcnt(0)
	s_barrier
	s_waitcnt vmcnt(3)
	v_mfma_f32_16x16x32_f16 v[84:87], v[2:5], v[46:49], v[18:21]
	v_mfma_f32_16x16x32_f16 v[88:91], v[14:17], v[46:49], v[38:41]
	ds_read_b128 v[56:59], v75 offset:0
	ds_read_b128 v[60:63], v75 offset:1024
	v_mfma_f32_16x16x32_f16 v[84:87], v[6:9], v[50:53], v[84:87]
	v_mfma_f32_16x16x32_f16 v[88:91], v[10:13], v[50:53], v[88:91]
	s_waitcnt lgkmcnt(1)
	v_mfma_f32_16x16x32_f16 v[84:87], v[30:33], v[56:59], v[84:87]
	v_mfma_f32_16x16x32_f16 v[88:91], v[22:25], v[56:59], v[88:91]
	s_waitcnt lgkmcnt(0)
	v_mfma_f32_16x16x32_f16 v[84:87], v[34:37], v[60:63], v[84:87]
	v_mfma_f32_16x16x32_f16 v[88:91], v[26:29], v[60:63], v[88:91]
	s_add_u32 s13, s12, 6
	s_min_u32 s13, s13, 450
	s_cmp_ge_u32 s14, s13
	s_cbranch_scc1 .Lca_ok_11
	s_mov_b32 s15, 0

.Lca_ok_11:
	buffer_load_dwordx4 v[46:49], v117, s[4:7], 0 offen offset:3072 sc1
	ds_read_b128 v[50:53], v116 offset:1024
	s_nop 1
	v_exp_f32_e32 v94, v86
	v_exp_f32_e32 v95, v90
	v_exp_f32_e32 v96, v84
	v_exp_f32_e32 v97, v88
	v_exp_f32_e32 v98, v85
	v_exp_f32_e32 v99, v89
	v_pk_add_f32 v[100:101], v[94:95], 1.0 op_sel_hi:[1,0]
	v_pk_fma_f32 v[102:103], v[94:95], s[8:9], v[92:93] op_sel_hi:[1,0,0]
	v_pk_fma_f32 v[100:101], v[96:97], v[100:101], v[100:101]
	v_pk_fma_f32 v[104:105], v[100:101], v[98:99], v[100:101]
	v_rcp_f32_e32 v104, v104
	v_rcp_f32_e32 v105, v105
	v_pk_fma_f32 v[102:103], v[102:103], v[98:99], v[102:103]
	v_pk_fma_f32 v[102:103], v[64:65], v[100:101], v[102:103]
	v_exp_f32_e32 v106, v87
	v_pk_mul_f32 v[64:65], v[102:103], v[104:105]
	v_exp_f32_e32 v108, v64
	v_exp_f32_e32 v109, v65
	v_exp_f32_e32 v107, v91
	v_pk_add_f32 v[110:111], v[108:109], 1.0 op_sel_hi:[1,0]
	v_pk_fma_f32 v[110:111], v[110:111], v[106:107], v[110:111]
	v_rcp_f32_e32 v110, v110
	v_rcp_f32_e32 v111, v111
	v_pk_add_f32 v[112:113], v[108:109], -1.0 op_sel_hi:[1,0]
	v_pk_mul_f32 v[112:113], v[112:113], v[110:111]
	v_cvt_pk_f16_f32 v114, v112, v113
	ds_write_b32 v81, v114 offset:2048
	s_waitcnt lgkmcnt(0)
	s_add_u32 s12, s12, 4
	v_add_u32_e32 v116, 0x400, v116
	v_add_u32_e32 v117, 0x1000, v117
	s_cmp_lt_u32 s12, 450
	s_cbranch_scc1 .Lca_loop
	s_barrier
	s_barrier
	s_barrier
	s_barrier
	s_endpgm

.Lk_232:
	s_waitcnt vmcnt(13)
	v_fma_mixlo_f16 v52, v46, v58, 0
	v_fma_mixlo_f16 v53, v46, v58, -v52 op_sel_hi:[0,0,1]
	v_cvt_f16_f32_e32 v58, v57
	v_cmp_eq_u32_e32 vcc, 1, v54
	v_cmp_gt_u32_e64 s[0:1], 16, v80
	v_cvt_f16_f32_e32 v64, v51
	v_cvt_f32_f16_e32 v60, v58
	v_cndmask_b32_e32 v53, 0, v53, vcc
	v_cndmask_b32_e64 v65, v53, v52, s[0:1]
	v_cvt_f32_f16_e32 v61, v64
	v_sub_f32_e32 v53, v57, v60
	v_cvt_f16_f32_e32 v53, v53
	v_cvt_f16_f32_e32 v57, v59
	v_cndmask_b32_e64 v67, 0, v52, s[0:1]
	v_sub_f32_e32 v51, v51, v61
	v_cndmask_b32_e32 v53, 0, v53, vcc
	v_cndmask_b32_e64 v66, v53, v58, s[0:1]
	v_cvt_f32_f16_e32 v53, v57
	v_cndmask_b32_e64 v68, 0, v58, s[0:1]
	s_waitcnt vmcnt(2)
	v_pk_mul_f32 v[16:17], v[46:47], v[16:17] op_sel_hi:[0,1]
	v_pk_mul_f32 v[18:19], v[46:47], v[18:19] op_sel_hi:[0,1]
	v_sub_f32_e32 v52, v59, v53
	v_cvt_f16_f32_e32 v69, v52
	global_load_dword v52, v[2:3], off offset:4
	global_load_dword v53, v[2:3], off offset:260
	global_load_dword v58, v[2:3], off offset:516
	global_load_dword v59, v[2:3], off offset:772
	global_load_dword v60, v[4:5], off offset:4
	global_load_dword v61, v[4:5], off offset:260
	global_load_dword v62, v[4:5], off offset:516
	global_load_dword v63, v[4:5], off offset:772
	v_pk_mul_f32 v[20:21], v[46:47], v[20:21] op_sel_hi:[0,1]
	v_pk_mul_f32 v[22:23], v[46:47], v[22:23] op_sel_hi:[0,1]
	v_pk_mul_f32 v[24:25], v[46:47], v[24:25] op_sel_hi:[0,1]
	v_pk_mul_f32 v[26:27], v[46:47], v[26:27] op_sel_hi:[0,1]
	v_cvt_pk_f16_f32 v16, v16, v17
	v_cvt_pk_f16_f32 v17, v18, v19
	v_pk_mul_f32 v[18:19], v[46:47], v[32:33] op_sel_hi:[0,1]
	v_pk_mul_f32 v[32:33], v[46:47], v[34:35] op_sel_hi:[0,1]
	v_cvt_pk_f16_f32 v20, v20, v21
	v_cvt_pk_f16_f32 v21, v22, v23
	v_pk_mul_f32 v[22:23], v[46:47], v[28:29] op_sel_hi:[0,1]
	v_pk_mul_f32 v[28:29], v[46:47], v[30:31] op_sel_hi:[0,1]
	v_cvt_pk_f16_f32 v24, v24, v25
	v_cvt_pk_f16_f32 v25, v26, v27
	v_cvt_f16_f32_e32 v26, v50
	v_cvt_pk_f16_f32 v18, v18, v19
	v_cvt_pk_f16_f32 v19, v32, v33
	v_cvt_pk_f16_f32 v22, v22, v23
	v_cvt_pk_f16_f32 v23, v28, v29
	v_cvt_f16_f32_e32 v29, v56
	v_cvt_f16_f32_e32 v32, v55
	v_cvt_f32_f16_e32 v30, v26
	v_cvt_f16_f32_e32 v51, v51
	v_cvt_f32_f16_e32 v31, v29
	v_cvt_f32_f16_e32 v33, v32
	v_sub_f32_e32 v30, v50, v30
	v_cvt_f16_f32_e32 v30, v30
	v_sub_f32_e32 v31, v56, v31
	v_sub_f32_e32 v33, v55, v33
	v_cvt_f16_f32_e32 v31, v31
	v_cvt_f16_f32_e32 v33, v33
	v_pk_mul_f32 v[12:13], v[46:47], v[12:13] op_sel_hi:[0,1]
	v_pk_mul_f32 v[14:15], v[46:47], v[14:15] op_sel_hi:[0,1]
	s_waitcnt vmcnt(8)
	v_fma_mixlo_f16 v27, v46, v45, 0
	v_cvt_pk_f16_f32 v12, v12, v13
	v_cvt_pk_f16_f32 v13, v14, v15
	v_pk_mul_f32 v[14:15], v[46:47], v[36:37] op_sel_hi:[0,1]
	v_pk_mul_f32 v[36:37], v[46:47], v[38:39] op_sel_hi:[0,1]
	v_fma_mixlo_f16 v28, v46, v45, -v27 op_sel_hi:[0,0,1]
	v_cndmask_b32_e32 v30, 0, v30, vcc
	v_cvt_pk_f16_f32 v14, v14, v15
	v_cvt_pk_f16_f32 v15, v36, v37
	v_cndmask_b32_e32 v28, 0, v28, vcc
	v_cndmask_b32_e64 v30, v30, v26, s[0:1]
	v_cndmask_b32_e32 v31, 0, v31, vcc
	v_cndmask_b32_e64 v36, 0, v26, s[0:1]
	v_cndmask_b32_e32 v26, 0, v33, vcc
	v_cndmask_b32_e32 v51, 0, v51, vcc
	v_cndmask_b32_e32 v2, 0, v69, vcc
	s_mov_b32 s8, 0x4038aa3b
	v_and_b32_e32 v34, 15, v0
	v_cndmask_b32_e64 v28, v28, v27, s[0:1]
	v_cndmask_b32_e64 v31, v31, v29, s[0:1]
	v_cndmask_b32_e64 v35, 0, v27, s[0:1]
	v_cndmask_b32_e64 v26, v26, v32, s[0:1]
	v_cndmask_b32_e64 v51, v51, v64, s[0:1]
	v_cndmask_b32_e64 v4, 0, v64, s[0:1]
	v_cndmask_b32_e64 v5, 0, v57, s[0:1]
	v_cndmask_b32_e64 v2, v2, v57, s[0:1]
	s_mov_b32 s9, 0xbfb8aa3b
	v_cndmask_b32_e64 v29, 0, v29, s[0:1]
	v_cndmask_b32_e64 v33, 0, v32, s[0:1]
	v_pack_b32_f16 v27, v31, v26
	v_pack_b32_f16 v26, v28, v30
	v_pack_b32_f16 v28, v35, v36
	s_lshl_b32 s0, s15, 8
	v_lshlrev_b32_e32 v81, 4, v34
	v_lshlrev_b32_e32 v35, 2, v54
	s_mov_b32 s7, 0
	v_pk_add_f32 v[6:7], v[6:7], v[8:9]
	v_pk_add_f32 v[8:9], v[10:11], v[48:49]
	s_mov_b32 s6, s9
	v_pk_mul_f32 v[10:11], v[46:47], v[40:41] op_sel_hi:[0,1]
	v_pk_mul_f32 v[40:41], v[46:47], v[42:43] op_sel_hi:[0,1]
	v_pack_b32_f16 v29, v29, v33
	v_lshlrev_b32_e32 v74, 4, v80
	v_or3_b32 v35, v81, v35, s0
	s_waitcnt vmcnt(2)
	v_pk_add_f32 v[30:31], v[52:53], v[60:61]
	v_pack_b32_f16 v3, v51, v2
	s_waitcnt vmcnt(0)
	v_pk_add_f32 v[32:33], v[58:59], v[62:63]
	v_pack_b32_f16 v2, v65, v66
	v_pack_b32_f16 v5, v4, v5
	v_pack_b32_f16 v4, v67, v68
	v_pk_mul_f32 v[8:9], v[8:9], s[8:9]
	v_pk_mul_f32 v[6:7], v[6:7], s[6:7] op_sel_hi:[1,0]
	v_cvt_pk_f16_f32 v10, v10, v11
	v_cvt_pk_f16_f32 v11, v40, v41
	v_pk_mul_f32 v[32:33], v[32:33], s[8:9]
	v_pk_mul_f32 v[30:31], v[30:31], s[6:7] op_sel_hi:[1,0]
	v_add_u32_e32 v78, 0x23280, v74
	v_add_u32_e32 v79, 0x23280, v35
	s_mov_b64 s[0:1], -1
	s_and_b64 vcc, exec, s[4:5]
	s_waitcnt lgkmcnt(0)
	s_barrier
	s_cbranch_vccz .Lk_298
	s_setprio 0
	v_and_b32_e32 v34, 15, v80
	v_lshrrev_b32_e32 v35, 4, v80
	s_and_b32 s10, s15, 1
	v_lshrrev_b32_e32 v36, 2, v34
	v_and_b32_e32 v37, 3, v34
	v_lshl_add_u32 v36, v36, 3, v37
	s_lshl_b32 s11, s10, 2
	v_add_u32_e32 v36, s11, v36
	v_lshlrev_b32_e32 v36, 9, v36
	v_lshl_add_u32 v36, v35, 5, v36
	global_load_dwordx4 v[44:47], v36, s[42:43] offset:0
	global_load_dwordx4 v[48:51], v36, s[42:43] offset:16
	global_load_dwordx4 v[52:55], v36, s[42:43] offset:128
	global_load_dwordx4 v[56:59], v36, s[42:43] offset:144
	global_load_dwordx4 v[60:63], v36, s[42:43] offset:256
	global_load_dwordx4 v[64:67], v36, s[42:43] offset:272
	global_load_dwordx4 v[68:71], v36, s[42:43] offset:384
	global_load_dwordx4 v[72:75], v36, s[42:43] offset:400
	v_lshlrev_b32_e32 v37, 5, v35
	s_lshl_b32 s12, s10, 4
	v_add_u32_e32 v37, s12, v37
	global_load_dwordx4 v[120:123], v37, s[44:45]
	s_mul_i32 s12, s3, 0x70800
	s_add_u32 s16, s22, s12
	s_addc_u32 s17, s23, 0
	s_lshl_b32 s12, s3, 8
	s_add_u32 s18, s24, s12
	s_addc_u32 s19, s25, 0
	s_add_u32 s18, s18, s11
	s_addc_u32 s19, s19, 0
	v_lshlrev_b32_e32 v38, 4, v80
	s_lshl_b32 s12, s10, 3
	v_add_u32_e32 v38, s12, v38
	v_lshlrev_b32_e32 v39, 2, v34
	v_add_u32_e32 v39, 0x1c200, v39
	s_mov_b32 s0, 0x4038aa3b
	s_mov_b32 s1, 0
	s_mov_b32 s9, 2
	s_waitcnt vmcnt(0)
	v_cvt_pk_f16_f32 v104, v44, v45
	v_cvt_pk_f16_f32 v105, v46, v47
	v_cvt_pk_f16_f32 v106, v48, v49
	v_cvt_pk_f16_f32 v107, v50, v51
	v_cvt_pk_f16_f32 v108, v52, v53
	v_cvt_pk_f16_f32 v109, v54, v55
	v_cvt_pk_f16_f32 v110, v56, v57
	v_cvt_pk_f16_f32 v111, v58, v59
	v_cvt_pk_f16_f32 v112, v60, v61
	v_cvt_pk_f16_f32 v113, v62, v63
	v_cvt_pk_f16_f32 v114, v64, v65
	v_cvt_pk_f16_f32 v115, v66, v67
	v_cvt_pk_f16_f32 v116, v68, v69
	v_cvt_pk_f16_f32 v117, v70, v71
	v_cvt_pk_f16_f32 v118, v72, v73
	v_cvt_pk_f16_f32 v119, v74, v75
	ds_read_b32 v64, v39
	v_mov_b32_e32 v40, 0
	v_mov_b32_e32 v41, 0
	v_mov_b32_e32 v61, 0
	v_mov_b32_e32 v63, 0
	v_mov_b32_e32 v83, 0
	v_mov_b32_e32 v58, 0xc038aa3b
	v_mov_b32_e32 v59, 0xc038aa3b
	s_waitcnt lgkmcnt(0)
	v_and_b32_e32 v60, 0xffff, v64
	v_lshrrev_b32_e32 v62, 16, v64
	s_nop 1
	v_mfma_f32_16x16x32_f16 v[50:53], v[2:5], v[60:63], v[6:9]
	v_mfma_f32_16x16x32_f16 v[54:57], v[26:29], v[60:63], v[30:33]
	ds_read_b128 v[42:45], v78 offset:6144
	ds_read_b128 v[46:49], v78 offset:7168
	s_waitcnt lgkmcnt(1)
	v_mfma_f32_16x16x32_f16 v[50:53], v[18:21], v[42:45], v[50:53]
	v_mfma_f32_16x16x32_f16 v[54:57], v[10:13], v[42:45], v[54:57]
	s_waitcnt lgkmcnt(0)
	v_mfma_f32_16x16x32_f16 v[50:53], v[22:25], v[46:49], v[50:53]
	v_mfma_f32_16x16x32_f16 v[54:57], v[14:17], v[46:49], v[54:57]
	ds_read_b32 v64, v39 offset:64
	s_nop 7
	v_exp_f32_e32 v84, v52
	v_exp_f32_e32 v85, v56
	v_exp_f32_e32 v86, v50
	v_exp_f32_e32 v87, v54
	v_exp_f32_e32 v88, v51
	v_exp_f32_e32 v89, v55
	v_pk_add_f32 v[90:91], v[84:85], 1.0 op_sel_hi:[1,0]
	v_pk_fma_f32 v[92:93], v[84:85], s[0:1], v[58:59] op_sel_hi:[1,0,0]
	v_pk_fma_f32 v[90:91], v[86:87], v[90:91], v[90:91]
	v_pk_fma_f32 v[94:95], v[90:91], v[88:89], v[90:91]
	v_rcp_f32_e32 v94, v94
	v_rcp_f32_e32 v95, v95
	v_pk_fma_f32 v[92:93], v[92:93], v[88:89], v[92:93]
	v_pk_fma_f32 v[92:93], v[40:41], v[90:91], v[92:93]
	v_exp_f32_e32 v96, v53
	v_pk_mul_f32 v[40:41], v[92:93], v[94:95]
	v_exp_f32_e32 v98, v40
	v_exp_f32_e32 v99, v41
	v_exp_f32_e32 v97, v57
	v_pk_add_f32 v[100:101], v[98:99], 1.0 op_sel_hi:[1,0]
	v_pk_fma_f32 v[100:101], v[100:101], v[96:97], v[100:101]
	v_rcp_f32_e32 v100, v100
	v_rcp_f32_e32 v101, v101
	v_pk_add_f32 v[102:103], v[98:99], -1.0 op_sel_hi:[1,0]
	v_pk_mul_f32 v[102:103], v[102:103], v[100:101]
	v_cvt_pk_f16_f32 v126, v102, v103
	ds_write_b32 v79, v126 offset:4096
	s_waitcnt lgkmcnt(1)
	v_and_b32_e32 v60, 0xffff, v64
	v_lshrrev_b32_e32 v62, 16, v64
	s_nop 1
	v_mfma_f32_16x16x32_f16 v[50:53], v[2:5], v[60:63], v[6:9]
	v_mfma_f32_16x16x32_f16 v[54:57], v[26:29], v[60:63], v[30:33]
	s_waitcnt lgkmcnt(0)
	s_barrier
	s_cmp_lt_u32 s15, 2
	s_cbranch_scc0 .Lpb_nc_1
	ds_read_b128 v[66:69], v78 offset:0
	ds_read_b128 v[70:73], v78 offset:1024
.Lpb_nc_1:
	ds_read_b128 v[42:45], v78 offset:4096
	ds_read_b128 v[46:49], v78 offset:5120
	s_waitcnt lgkmcnt(1)
	v_mfma_f32_16x16x32_f16 v[50:53], v[18:21], v[42:45], v[50:53]
	v_mfma_f32_16x16x32_f16 v[54:57], v[10:13], v[42:45], v[54:57]
	s_waitcnt lgkmcnt(0)
	v_mfma_f32_16x16x32_f16 v[50:53], v[22:25], v[46:49], v[50:53]
	v_mfma_f32_16x16x32_f16 v[54:57], v[14:17], v[46:49], v[54:57]
	ds_read_b32 v64, v39 offset:128
	s_cmp_lt_u32 s15, 2
	s_cbranch_scc0 .Lpb_np_2
	v_mfma_f32_16x16x32_f16 v[74:77], v[104:107], v[66:69], v[120:123]
	v_mfma_f32_16x16x32_f16 v[74:77], v[108:111], v[70:73], v[74:77]
	v_mfma_f32_16x16x32_f16 v[74:77], v[112:115], v[42:45], v[74:77]
	v_mfma_f32_16x16x32_f16 v[74:77], v[116:119], v[46:49], v[74:77]
	s_nop 7
	v_cvt_pk_f16_f32 v124, v74, v75
	v_cvt_pk_f16_f32 v125, v76, v77
	global_store_dwordx2 v38, v[124:125], s[16:17] offset:0 sc1
	s_waitcnt vmcnt(4)
	s_mov_b32 s10, 0
	v_mov_b32_e32 v82, s10
	s_mov_b64 s[12:13], exec
	s_mov_b64 exec, 1
	global_store_dword v83, v82, s[18:19] sc1
	s_mov_b64 exec, s[12:13]
.Lpb_np_2:
	s_nop 7
	v_exp_f32_e32 v84, v52
	v_exp_f32_e32 v85, v56
	v_exp_f32_e32 v86, v50
	v_exp_f32_e32 v87, v54
	v_exp_f32_e32 v88, v51
	v_exp_f32_e32 v89, v55
	v_pk_add_f32 v[90:91], v[84:85], 1.0 op_sel_hi:[1,0]
	v_pk_fma_f32 v[92:93], v[84:85], s[0:1], v[58:59] op_sel_hi:[1,0,0]
	v_pk_fma_f32 v[90:91], v[86:87], v[90:91], v[90:91]
	v_pk_fma_f32 v[94:95], v[90:91], v[88:89], v[90:91]
	v_rcp_f32_e32 v94, v94
	v_rcp_f32_e32 v95, v95
	v_pk_fma_f32 v[92:93], v[92:93], v[88:89], v[92:93]
	v_pk_fma_f32 v[92:93], v[40:41], v[90:91], v[92:93]
	v_exp_f32_e32 v96, v53
	v_pk_mul_f32 v[40:41], v[92:93], v[94:95]
	v_exp_f32_e32 v98, v40
	v_exp_f32_e32 v99, v41
	v_exp_f32_e32 v97, v57
	v_pk_add_f32 v[100:101], v[98:99], 1.0 op_sel_hi:[1,0]
	v_pk_fma_f32 v[100:101], v[100:101], v[96:97], v[100:101]
	v_rcp_f32_e32 v100, v100
	v_rcp_f32_e32 v101, v101
	v_pk_add_f32 v[102:103], v[98:99], -1.0 op_sel_hi:[1,0]
	v_pk_mul_f32 v[102:103], v[102:103], v[100:101]
	v_cvt_pk_f16_f32 v126, v102, v103
	ds_write_b32 v79, v126 offset:6144
	s_waitcnt lgkmcnt(1)
	v_and_b32_e32 v60, 0xffff, v64
	v_lshrrev_b32_e32 v62, 16, v64
	s_nop 1
	v_mfma_f32_16x16x32_f16 v[50:53], v[2:5], v[60:63], v[6:9]
	v_mfma_f32_16x16x32_f16 v[54:57], v[26:29], v[60:63], v[30:33]
	s_waitcnt lgkmcnt(0)
	v_add_u32_e32 v39, 0x80, v39
	v_add_u32_e32 v38, 0x400, v38

.Lpb_nc_3:
	ds_read_b128 v[42:45], v78 offset:6144
	ds_read_b128 v[46:49], v78 offset:7168
	s_waitcnt lgkmcnt(1)
	v_mfma_f32_16x16x32_f16 v[50:53], v[18:21], v[42:45], v[50:53]
	v_mfma_f32_16x16x32_f16 v[54:57], v[10:13], v[42:45], v[54:57]
	s_waitcnt lgkmcnt(0)
	v_mfma_f32_16x16x32_f16 v[50:53], v[22:25], v[46:49], v[50:53]
	v_mfma_f32_16x16x32_f16 v[54:57], v[14:17], v[46:49], v[54:57]
	ds_read_b32 v64, v39 offset:64
	s_cmp_lt_u32 s15, 2
	s_cbranch_scc0 .Lpb_np_4
	v_mfma_f32_16x16x32_f16 v[74:77], v[104:107], v[66:69], v[120:123]
	v_mfma_f32_16x16x32_f16 v[74:77], v[108:111], v[70:73], v[74:77]
	v_mfma_f32_16x16x32_f16 v[74:77], v[112:115], v[42:45], v[74:77]
	v_mfma_f32_16x16x32_f16 v[74:77], v[116:119], v[46:49], v[74:77]
	s_nop 7
	v_cvt_pk_f16_f32 v124, v74, v75
	v_cvt_pk_f16_f32 v125, v76, v77
	global_store_dwordx2 v38, v[124:125], s[16:17] offset:0 sc1
	s_waitcnt vmcnt(4)
	s_add_i32 s10, s9, -2
	s_max_i32 s10, s10, 0
	v_mov_b32_e32 v82, s10
	s_mov_b64 s[12:13], exec
	s_mov_b64 exec, 1
	global_store_dword v83, v82, s[18:19] sc1
	s_mov_b64 exec, s[12:13]
.Lpb_np_4:
	s_nop 7
	v_min_f32_e32 v40, 0x42700000, v40
	v_min_f32_e32 v41, 0x42700000, v41
	v_exp_f32_e32 v84, v52
	v_exp_f32_e32 v85, v56
	v_exp_f32_e32 v86, v50
	v_exp_f32_e32 v87, v54
	v_exp_f32_e32 v88, v51
	v_exp_f32_e32 v89, v55
	v_pk_add_f32 v[90:91], v[84:85], 1.0 op_sel_hi:[1,0]
	v_pk_fma_f32 v[92:93], v[84:85], s[0:1], v[58:59] op_sel_hi:[1,0,0]
	v_pk_fma_f32 v[90:91], v[86:87], v[90:91], v[90:91]
	v_pk_fma_f32 v[94:95], v[90:91], v[88:89], v[90:91]
	v_rcp_f32_e32 v94, v94
	v_rcp_f32_e32 v95, v95
	v_pk_fma_f32 v[92:93], v[92:93], v[88:89], v[92:93]
	v_pk_fma_f32 v[92:93], v[40:41], v[90:91], v[92:93]
	v_exp_f32_e32 v96, v53
	v_pk_mul_f32 v[40:41], v[92:93], v[94:95]
	v_exp_f32_e32 v98, v40
	v_exp_f32_e32 v99, v41
	v_exp_f32_e32 v97, v57
	v_pk_add_f32 v[100:101], v[98:99], 1.0 op_sel_hi:[1,0]
	v_pk_fma_f32 v[100:101], v[100:101], v[96:97], v[100:101]
	v_rcp_f32_e32 v100, v100
	v_rcp_f32_e32 v101, v101
	v_pk_add_f32 v[102:103], v[98:99], -1.0 op_sel_hi:[1,0]
	v_pk_mul_f32 v[102:103], v[102:103], v[100:101]
	v_cvt_pk_f16_f32 v126, v102, v103
	ds_write_b32 v79, v126 offset:4096
	s_waitcnt lgkmcnt(1)
	v_and_b32_e32 v60, 0xffff, v64
	v_lshrrev_b32_e32 v62, 16, v64
	s_nop 1
	v_mfma_f32_16x16x32_f16 v[50:53], v[2:5], v[60:63], v[6:9]
	v_mfma_f32_16x16x32_f16 v[54:57], v[26:29], v[60:63], v[30:33]
	s_waitcnt lgkmcnt(0)
	s_barrier
	s_cmp_lt_u32 s15, 2
	s_cbranch_scc0 .Lpb_nc_5
	ds_read_b128 v[66:69], v78 offset:0
	ds_read_b128 v[70:73], v78 offset:1024
.Lpb_nc_5:
	ds_read_b128 v[42:45], v78 offset:4096
	ds_read_b128 v[46:49], v78 offset:5120
	s_waitcnt lgkmcnt(1)
	v_mfma_f32_16x16x32_f16 v[50:53], v[18:21], v[42:45], v[50:53]
	v_mfma_f32_16x16x32_f16 v[54:57], v[10:13], v[42:45], v[54:57]
	s_waitcnt lgkmcnt(0)
	v_mfma_f32_16x16x32_f16 v[50:53], v[22:25], v[46:49], v[50:53]
	v_mfma_f32_16x16x32_f16 v[54:57], v[14:17], v[46:49], v[54:57]
	ds_read_b32 v64, v39 offset:128
	s_cmp_lt_u32 s15, 2
	s_cbranch_scc0 .Lpb_np_6
	v_mfma_f32_16x16x32_f16 v[74:77], v[104:107], v[66:69], v[120:123]
	v_mfma_f32_16x16x32_f16 v[74:77], v[108:111], v[70:73], v[74:77]
	v_mfma_f32_16x16x32_f16 v[74:77], v[112:115], v[42:45], v[74:77]
	v_mfma_f32_16x16x32_f16 v[74:77], v[116:119], v[46:49], v[74:77]
	s_nop 7
	v_cvt_pk_f16_f32 v124, v74, v75
	v_cvt_pk_f16_f32 v125, v76, v77
	global_store_dwordx2 v38, v[124:125], s[16:17] offset:1024 sc1
	s_waitcnt vmcnt(4)
	s_add_i32 s10, s9, -1
	s_max_i32 s10, s10, 0
	v_mov_b32_e32 v82, s10
	s_mov_b64 s[12:13], exec
	s_mov_b64 exec, 1
	global_store_dword v83, v82, s[18:19] sc1
	s_mov_b64 exec, s[12:13]
.Lpb_np_6:
	s_nop 7
	v_exp_f32_e32 v84, v52
	v_exp_f32_e32 v85, v56
	v_exp_f32_e32 v86, v50
	v_exp_f32_e32 v87, v54
	v_exp_f32_e32 v88, v51
	v_exp_f32_e32 v89, v55
	v_pk_add_f32 v[90:91], v[84:85], 1.0 op_sel_hi:[1,0]
	v_pk_fma_f32 v[92:93], v[84:85], s[0:1], v[58:59] op_sel_hi:[1,0,0]
	v_pk_fma_f32 v[90:91], v[86:87], v[90:91], v[90:91]
	v_pk_fma_f32 v[94:95], v[90:91], v[88:89], v[90:91]
	v_rcp_f32_e32 v94, v94
	v_rcp_f32_e32 v95, v95
	v_pk_fma_f32 v[92:93], v[92:93], v[88:89], v[92:93]
	v_pk_fma_f32 v[92:93], v[40:41], v[90:91], v[92:93]
	v_exp_f32_e32 v96, v53
	v_pk_mul_f32 v[40:41], v[92:93], v[94:95]
	v_exp_f32_e32 v98, v40
	v_exp_f32_e32 v99, v41
	v_exp_f32_e32 v97, v57
	v_pk_add_f32 v[100:101], v[98:99], 1.0 op_sel_hi:[1,0]
	v_pk_fma_f32 v[100:101], v[100:101], v[96:97], v[100:101]
	v_rcp_f32_e32 v100, v100
	v_rcp_f32_e32 v101, v101
	v_pk_add_f32 v[102:103], v[98:99], -1.0 op_sel_hi:[1,0]
	v_pk_mul_f32 v[102:103], v[102:103], v[100:101]
	v_cvt_pk_f16_f32 v126, v102, v103
	ds_write_b32 v79, v126 offset:6144
	s_waitcnt lgkmcnt(1)
	v_and_b32_e32 v60, 0xffff, v64
	v_lshrrev_b32_e32 v62, 16, v64
	s_nop 1
	v_mfma_f32_16x16x32_f16 v[50:53], v[2:5], v[60:63], v[6:9]
	v_mfma_f32_16x16x32_f16 v[54:57], v[26:29], v[60:63], v[30:33]
	s_waitcnt lgkmcnt(0)
	s_barrier
	s_cmp_lt_u32 s15, 2
	s_cbranch_scc0 .Lpb_nc_7
	ds_read_b128 v[66:69], v78 offset:2048
	ds_read_b128 v[70:73], v78 offset:3072
.Lpb_nc_7:
	ds_read_b128 v[42:45], v78 offset:6144
	ds_read_b128 v[46:49], v78 offset:7168
	s_waitcnt lgkmcnt(1)
	v_mfma_f32_16x16x32_f16 v[50:53], v[18:21], v[42:45], v[50:53]
	v_mfma_f32_16x16x32_f16 v[54:57], v[10:13], v[42:45], v[54:57]
	s_waitcnt lgkmcnt(0)
	v_mfma_f32_16x16x32_f16 v[50:53], v[22:25], v[46:49], v[50:53]
	v_mfma_f32_16x16x32_f16 v[54:57], v[14:17], v[46:49], v[54:57]
	ds_read_b32 v64, v39 offset:192
	s_cmp_lt_u32 s15, 2
	s_cbranch_scc0 .Lpb_np_8
	v_mfma_f32_16x16x32_f16 v[74:77], v[104:107], v[66:69], v[120:123]
	v_mfma_f32_16x16x32_f16 v[74:77], v[108:111], v[70:73], v[74:77]
	v_mfma_f32_16x16x32_f16 v[74:77], v[112:115], v[42:45], v[74:77]
	v_mfma_f32_16x16x32_f16 v[74:77], v[116:119], v[46:49], v[74:77]
	s_nop 7
	v_cvt_pk_f16_f32 v124, v74, v75
	v_cvt_pk_f16_f32 v125, v76, v77
	global_store_dwordx2 v38, v[124:125], s[16:17] offset:2048 sc1
	s_waitcnt vmcnt(4)
	s_add_i32 s10, s9, 0
	s_max_i32 s10, s10, 0
	v_mov_b32_e32 v82, s10
	s_mov_b64 s[12:13], exec
	s_mov_b64 exec, 1
	global_store_dword v83, v82, s[18:19] sc1
	s_mov_b64 exec, s[12:13]
.Lpb_np_8:
	s_nop 7
	v_exp_f32_e32 v84, v52
	v_exp_f32_e32 v85, v56
	v_exp_f32_e32 v86, v50
	v_exp_f32_e32 v87, v54
	v_exp_f32_e32 v88, v51
	v_exp_f32_e32 v89, v55
	v_pk_add_f32 v[90:91], v[84:85], 1.0 op_sel_hi:[1,0]
	v_pk_fma_f32 v[92:93], v[84:85], s[0:1], v[58:59] op_sel_hi:[1,0,0]
	v_pk_fma_f32 v[90:91], v[86:87], v[90:91], v[90:91]
	v_pk_fma_f32 v[94:95], v[90:91], v[88:89], v[90:91]
	v_rcp_f32_e32 v94, v94
	v_rcp_f32_e32 v95, v95
	v_pk_fma_f32 v[92:93], v[92:93], v[88:89], v[92:93]
	v_pk_fma_f32 v[92:93], v[40:41], v[90:91], v[92:93]
	v_exp_f32_e32 v96, v53
	v_pk_mul_f32 v[40:41], v[92:93], v[94:95]
	v_exp_f32_e32 v98, v40
	v_exp_f32_e32 v99, v41
	v_exp_f32_e32 v97, v57
	v_pk_add_f32 v[100:101], v[98:99], 1.0 op_sel_hi:[1,0]
	v_pk_fma_f32 v[100:101], v[100:101], v[96:97], v[100:101]
	v_rcp_f32_e32 v100, v100
	v_rcp_f32_e32 v101, v101
	v_pk_add_f32 v[102:103], v[98:99], -1.0 op_sel_hi:[1,0]
	v_pk_mul_f32 v[102:103], v[102:103], v[100:101]
	v_cvt_pk_f16_f32 v126, v102, v103
	ds_write_b32 v79, v126 offset:4096
	s_waitcnt lgkmcnt(1)
	v_and_b32_e32 v60, 0xffff, v64
	v_lshrrev_b32_e32 v62, 16, v64
	s_nop 1
	v_mfma_f32_16x16x32_f16 v[50:53], v[2:5], v[60:63], v[6:9]
	v_mfma_f32_16x16x32_f16 v[54:57], v[26:29], v[60:63], v[30:33]
	s_waitcnt lgkmcnt(0)
	s_barrier
	s_cmp_lt_u32 s15, 2
	s_cbranch_scc0 .Lpb_nc_9
	ds_read_b128 v[66:69], v78 offset:0
	ds_read_b128 v[70:73], v78 offset:1024
.Lpb_nc_9:
	ds_read_b128 v[42:45], v78 offset:4096
	ds_read_b128 v[46:49], v78 offset:5120
	s_waitcnt lgkmcnt(1)
	v_mfma_f32_16x16x32_f16 v[50:53], v[18:21], v[42:45], v[50:53]
	v_mfma_f32_16x16x32_f16 v[54:57], v[10:13], v[42:45], v[54:57]
	s_waitcnt lgkmcnt(0)
	v_mfma_f32_16x16x32_f16 v[50:53], v[22:25], v[46:49], v[50:53]
	v_mfma_f32_16x16x32_f16 v[54:57], v[14:17], v[46:49], v[54:57]
	ds_read_b32 v64, v39 offset:256
	s_cmp_lt_u32 s15, 2
	s_cbranch_scc0 .Lpb_np_10
	v_mfma_f32_16x16x32_f16 v[74:77], v[104:107], v[66:69], v[120:123]
	v_mfma_f32_16x16x32_f16 v[74:77], v[108:111], v[70:73], v[74:77]
	v_mfma_f32_16x16x32_f16 v[74:77], v[112:115], v[42:45], v[74:77]
	v_mfma_f32_16x16x32_f16 v[74:77], v[116:119], v[46:49], v[74:77]
	s_nop 7
	v_cvt_pk_f16_f32 v124, v74, v75
	v_cvt_pk_f16_f32 v125, v76, v77
	global_store_dwordx2 v38, v[124:125], s[16:17] offset:3072 sc1
	s_waitcnt vmcnt(4)
	s_add_i32 s10, s9, 1
	s_max_i32 s10, s10, 0
	v_mov_b32_e32 v82, s10
	s_mov_b64 s[12:13], exec
	s_mov_b64 exec, 1
	global_store_dword v83, v82, s[18:19] sc1
	s_mov_b64 exec, s[12:13]
.Lpb_np_10:
	s_nop 7
	v_exp_f32_e32 v84, v52
	v_exp_f32_e32 v85, v56
	v_exp_f32_e32 v86, v50
	v_exp_f32_e32 v87, v54
	v_exp_f32_e32 v88, v51
	v_exp_f32_e32 v89, v55
	v_pk_add_f32 v[90:91], v[84:85], 1.0 op_sel_hi:[1,0]
	v_pk_fma_f32 v[92:93], v[84:85], s[0:1], v[58:59] op_sel_hi:[1,0,0]
	v_pk_fma_f32 v[90:91], v[86:87], v[90:91], v[90:91]
	v_pk_fma_f32 v[94:95], v[90:91], v[88:89], v[90:91]
	v_rcp_f32_e32 v94, v94
	v_rcp_f32_e32 v95, v95
	v_pk_fma_f32 v[92:93], v[92:93], v[88:89], v[92:93]
	v_pk_fma_f32 v[92:93], v[40:41], v[90:91], v[92:93]
	v_exp_f32_e32 v96, v53
	v_pk_mul_f32 v[40:41], v[92:93], v[94:95]
	v_exp_f32_e32 v98, v40
	v_exp_f32_e32 v99, v41
	v_exp_f32_e32 v97, v57
	v_pk_add_f32 v[100:101], v[98:99], 1.0 op_sel_hi:[1,0]
	v_pk_fma_f32 v[100:101], v[100:101], v[96:97], v[100:101]
	v_rcp_f32_e32 v100, v100
	v_rcp_f32_e32 v101, v101
	v_pk_add_f32 v[102:103], v[98:99], -1.0 op_sel_hi:[1,0]
	v_pk_mul_f32 v[102:103], v[102:103], v[100:101]
	v_cvt_pk_f16_f32 v126, v102, v103
	ds_write_b32 v79, v126 offset:6144
	s_waitcnt lgkmcnt(1)
	v_and_b32_e32 v60, 0xffff, v64
	v_lshrrev_b32_e32 v62, 16, v64
	s_nop 1
	v_mfma_f32_16x16x32_f16 v[50:53], v[2:5], v[60:63], v[6:9]
	v_mfma_f32_16x16x32_f16 v[54:57], v[26:29], v[60:63], v[30:33]
	s_waitcnt lgkmcnt(0)
	s_add_u32 s9, s9, 4
	v_add_u32_e32 v39, 0x100, v39
	v_add_u32_e32 v38, 0x1000, v38
	s_cmp_lt_u32 s9, 450
	s_cbranch_scc1 .Lpb_loop
	s_barrier
	s_cmp_lt_u32 s15, 2
	s_cbranch_scc0 .Lpb_nc_11
	ds_read_b128 v[66:69], v78 offset:2048
	ds_read_b128 v[70:73], v78 offset:3072

.Lk_298:
	s_and_b64 vcc, exec, s[0:1]
	s_cbranch_vccz .Lk_313
	s_setprio 2
	ds_read_b128 v[34:37], v81
	v_mov_b32_e32 v40, 0
	v_mov_b32_e32 v41, 0
	s_mov_b32 s0, 0x4038aa3b
	s_mov_b32 s1, 0
	v_mov_b32_e32 v58, 0xc038aa3b
	v_mov_b32_e32 v59, 0xc038aa3b
	v_mov_b32_e32 v39, v81
	s_mov_b32 s9, 2
	s_waitcnt lgkmcnt(0)
	ds_read_b128 v[42:45], v78 offset:2048
	ds_read_b128 v[46:49], v78 offset:3072
	v_mfma_f32_16x16x32_f16 v[50:53], v[2:5], v[34:37], v[6:9]
	v_mfma_f32_16x16x32_f16 v[54:57], v[26:29], v[34:37], v[30:33]
	s_waitcnt lgkmcnt(1)
	v_mfma_f32_16x16x32_f16 v[50:53], v[18:21], v[42:45], v[50:53]
	v_mfma_f32_16x16x32_f16 v[54:57], v[10:13], v[42:45], v[54:57]
	s_waitcnt lgkmcnt(0)
	v_mfma_f32_16x16x32_f16 v[50:53], v[22:25], v[46:49], v[50:53]
	v_mfma_f32_16x16x32_f16 v[54:57], v[14:17], v[46:49], v[54:57]
	ds_read_b128 v[34:37], v39 offset:256
	s_nop 6
	v_exp_f32_e32 v84, v52
	v_exp_f32_e32 v85, v56
	v_exp_f32_e32 v86, v50
	v_exp_f32_e32 v87, v54
	v_exp_f32_e32 v88, v51
	v_exp_f32_e32 v89, v55
	v_pk_add_f32 v[90:91], v[84:85], 1.0 op_sel_hi:[1,0]
	v_pk_fma_f32 v[92:93], v[84:85], s[0:1], v[58:59] op_sel_hi:[1,0,0]
	v_pk_fma_f32 v[90:91], v[86:87], v[90:91], v[90:91]
	v_pk_fma_f32 v[94:95], v[90:91], v[88:89], v[90:91]
	v_rcp_f32_e32 v94, v94
	v_rcp_f32_e32 v95, v95
	v_pk_fma_f32 v[92:93], v[92:93], v[88:89], v[92:93]
	v_pk_fma_f32 v[92:93], v[40:41], v[90:91], v[92:93]
	v_exp_f32_e32 v96, v53
	v_pk_mul_f32 v[40:41], v[92:93], v[94:95]
	v_exp_f32_e32 v98, v40
	v_exp_f32_e32 v99, v41
	v_exp_f32_e32 v97, v57
	v_pk_add_f32 v[100:101], v[98:99], 1.0 op_sel_hi:[1,0]
	v_pk_fma_f32 v[100:101], v[100:101], v[96:97], v[100:101]
	v_rcp_f32_e32 v100, v100
	v_rcp_f32_e32 v101, v101
	v_pk_add_f32 v[102:103], v[98:99], -1.0 op_sel_hi:[1,0]
	v_pk_mul_f32 v[102:103], v[102:103], v[100:101]
	v_cvt_pk_f16_f32 v104, v102, v103
	ds_write_b32 v79, v104 offset:0
	s_waitcnt lgkmcnt(0)
	s_barrier
	ds_read_b128 v[42:45], v78 offset:0
	ds_read_b128 v[46:49], v78 offset:1024
	v_mfma_f32_16x16x32_f16 v[50:53], v[2:5], v[34:37], v[6:9]
	v_mfma_f32_16x16x32_f16 v[54:57], v[26:29], v[34:37], v[30:33]
	s_waitcnt lgkmcnt(1)
	v_mfma_f32_16x16x32_f16 v[50:53], v[18:21], v[42:45], v[50:53]
	v_mfma_f32_16x16x32_f16 v[54:57], v[10:13], v[42:45], v[54:57]
	s_waitcnt lgkmcnt(0)
	v_mfma_f32_16x16x32_f16 v[50:53], v[22:25], v[46:49], v[50:53]
	v_mfma_f32_16x16x32_f16 v[54:57], v[14:17], v[46:49], v[54:57]
	ds_read_b128 v[34:37], v39 offset:512
	s_nop 6
	v_exp_f32_e32 v84, v52
	v_exp_f32_e32 v85, v56
	v_exp_f32_e32 v86, v50
	v_exp_f32_e32 v87, v54
	v_exp_f32_e32 v88, v51
	v_exp_f32_e32 v89, v55
	v_pk_add_f32 v[90:91], v[84:85], 1.0 op_sel_hi:[1,0]
	v_pk_fma_f32 v[92:93], v[84:85], s[0:1], v[58:59] op_sel_hi:[1,0,0]
	v_pk_fma_f32 v[90:91], v[86:87], v[90:91], v[90:91]
	v_pk_fma_f32 v[94:95], v[90:91], v[88:89], v[90:91]
	v_rcp_f32_e32 v94, v94
	v_rcp_f32_e32 v95, v95
	v_pk_fma_f32 v[92:93], v[92:93], v[88:89], v[92:93]
	v_pk_fma_f32 v[92:93], v[40:41], v[90:91], v[92:93]
	v_exp_f32_e32 v96, v53
	v_pk_mul_f32 v[40:41], v[92:93], v[94:95]
	v_exp_f32_e32 v98, v40
	v_exp_f32_e32 v99, v41
	v_exp_f32_e32 v97, v57
	v_pk_add_f32 v[100:101], v[98:99], 1.0 op_sel_hi:[1,0]
	v_pk_fma_f32 v[100:101], v[100:101], v[96:97], v[100:101]
	v_rcp_f32_e32 v100, v100
	v_rcp_f32_e32 v101, v101
	v_pk_add_f32 v[102:103], v[98:99], -1.0 op_sel_hi:[1,0]
	v_pk_mul_f32 v[102:103], v[102:103], v[100:101]
	v_cvt_pk_f16_f32 v104, v102, v103
	ds_write_b32 v79, v104 offset:2048
	s_waitcnt lgkmcnt(0)
	v_add_u32_e32 v39, 0x200, v39
.Lpa_loop:
	s_barrier
	ds_read_b128 v[42:45], v78 offset:2048
	ds_read_b128 v[46:49], v78 offset:3072
	v_mfma_f32_16x16x32_f16 v[50:53], v[2:5], v[34:37], v[6:9]
	v_mfma_f32_16x16x32_f16 v[54:57], v[26:29], v[34:37], v[30:33]
	s_waitcnt lgkmcnt(1)
	v_mfma_f32_16x16x32_f16 v[50:53], v[18:21], v[42:45], v[50:53]
	v_mfma_f32_16x16x32_f16 v[54:57], v[10:13], v[42:45], v[54:57]
	s_waitcnt lgkmcnt(0)
	v_mfma_f32_16x16x32_f16 v[50:53], v[22:25], v[46:49], v[50:53]
	v_mfma_f32_16x16x32_f16 v[54:57], v[14:17], v[46:49], v[54:57]
	ds_read_b128 v[34:37], v39 offset:256
	s_nop 6
	v_min_f32_e32 v40, 0x42700000, v40
	v_min_f32_e32 v41, 0x42700000, v41
	v_exp_f32_e32 v84, v52
	v_exp_f32_e32 v85, v56
	v_exp_f32_e32 v86, v50
	v_exp_f32_e32 v87, v54
	v_exp_f32_e32 v88, v51
	v_exp_f32_e32 v89, v55
	v_pk_add_f32 v[90:91], v[84:85], 1.0 op_sel_hi:[1,0]
	v_pk_fma_f32 v[92:93], v[84:85], s[0:1], v[58:59] op_sel_hi:[1,0,0]
	v_pk_fma_f32 v[90:91], v[86:87], v[90:91], v[90:91]
	v_pk_fma_f32 v[94:95], v[90:91], v[88:89], v[90:91]
	v_rcp_f32_e32 v94, v94
	v_rcp_f32_e32 v95, v95
	v_pk_fma_f32 v[92:93], v[92:93], v[88:89], v[92:93]
	v_pk_fma_f32 v[92:93], v[40:41], v[90:91], v[92:93]
	v_exp_f32_e32 v96, v53
	v_pk_mul_f32 v[40:41], v[92:93], v[94:95]
	v_exp_f32_e32 v98, v40
	v_exp_f32_e32 v99, v41
	v_exp_f32_e32 v97, v57
	v_pk_add_f32 v[100:101], v[98:99], 1.0 op_sel_hi:[1,0]
	v_pk_fma_f32 v[100:101], v[100:101], v[96:97], v[100:101]
	v_rcp_f32_e32 v100, v100
	v_rcp_f32_e32 v101, v101
	v_pk_add_f32 v[102:103], v[98:99], -1.0 op_sel_hi:[1,0]
	v_pk_mul_f32 v[102:103], v[102:103], v[100:101]
	v_cvt_pk_f16_f32 v104, v102, v103
	ds_write_b32 v79, v104 offset:0
	s_waitcnt lgkmcnt(0)
	s_barrier
	ds_read_b128 v[42:45], v78 offset:0
	ds_read_b128 v[46:49], v78 offset:1024
	v_mfma_f32_16x16x32_f16 v[50:53], v[2:5], v[34:37], v[6:9]
	v_mfma_f32_16x16x32_f16 v[54:57], v[26:29], v[34:37], v[30:33]
	s_waitcnt lgkmcnt(1)
	v_mfma_f32_16x16x32_f16 v[50:53], v[18:21], v[42:45], v[50:53]
	v_mfma_f32_16x16x32_f16 v[54:57], v[10:13], v[42:45], v[54:57]
	s_waitcnt lgkmcnt(0)
	v_mfma_f32_16x16x32_f16 v[50:53], v[22:25], v[46:49], v[50:53]
	v_mfma_f32_16x16x32_f16 v[54:57], v[14:17], v[46:49], v[54:57]
	ds_read_b128 v[34:37], v39 offset:512
	s_nop 6
	v_exp_f32_e32 v84, v52
	v_exp_f32_e32 v85, v56
	v_exp_f32_e32 v86, v50
	v_exp_f32_e32 v87, v54
	v_exp_f32_e32 v88, v51
	v_exp_f32_e32 v89, v55
	v_pk_add_f32 v[90:91], v[84:85], 1.0 op_sel_hi:[1,0]
	v_pk_fma_f32 v[92:93], v[84:85], s[0:1], v[58:59] op_sel_hi:[1,0,0]
	v_pk_fma_f32 v[90:91], v[86:87], v[90:91], v[90:91]
	v_pk_fma_f32 v[94:95], v[90:91], v[88:89], v[90:91]
	v_rcp_f32_e32 v94, v94
	v_rcp_f32_e32 v95, v95
	v_pk_fma_f32 v[92:93], v[92:93], v[88:89], v[92:93]
	v_pk_fma_f32 v[92:93], v[40:41], v[90:91], v[92:93]
	v_exp_f32_e32 v96, v53
	v_pk_mul_f32 v[40:41], v[92:93], v[94:95]
	v_exp_f32_e32 v98, v40
	v_exp_f32_e32 v99, v41
	v_exp_f32_e32 v97, v57
	v_pk_add_f32 v[100:101], v[98:99], 1.0 op_sel_hi:[1,0]
	v_pk_fma_f32 v[100:101], v[100:101], v[96:97], v[100:101]
	v_rcp_f32_e32 v100, v100
	v_rcp_f32_e32 v101, v101
	v_pk_add_f32 v[102:103], v[98:99], -1.0 op_sel_hi:[1,0]
	v_pk_mul_f32 v[102:103], v[102:103], v[100:101]
	v_cvt_pk_f16_f32 v104, v102, v103
	ds_write_b32 v79, v104 offset:2048
	s_waitcnt lgkmcnt(0)
	s_barrier
	ds_read_b128 v[42:45], v78 offset:2048
	ds_read_b128 v[46:49], v78 offset:3072
	v_mfma_f32_16x16x32_f16 v[50:53], v[2:5], v[34:37], v[6:9]
	v_mfma_f32_16x16x32_f16 v[54:57], v[26:29], v[34:37], v[30:33]
	s_waitcnt lgkmcnt(1)
	v_mfma_f32_16x16x32_f16 v[50:53], v[18:21], v[42:45], v[50:53]
	v_mfma_f32_16x16x32_f16 v[54:57], v[10:13], v[42:45], v[54:57]
	s_waitcnt lgkmcnt(0)
	v_mfma_f32_16x16x32_f16 v[50:53], v[22:25], v[46:49], v[50:53]
	v_mfma_f32_16x16x32_f16 v[54:57], v[14:17], v[46:49], v[54:57]
	ds_read_b128 v[34:37], v39 offset:768
	s_nop 6
	v_exp_f32_e32 v84, v52
	v_exp_f32_e32 v85, v56
	v_exp_f32_e32 v86, v50
	v_exp_f32_e32 v87, v54
	v_exp_f32_e32 v88, v51
	v_exp_f32_e32 v89, v55
	v_pk_add_f32 v[90:91], v[84:85], 1.0 op_sel_hi:[1,0]
	v_pk_fma_f32 v[92:93], v[84:85], s[0:1], v[58:59] op_sel_hi:[1,0,0]
	v_pk_fma_f32 v[90:91], v[86:87], v[90:91], v[90:91]
	v_pk_fma_f32 v[94:95], v[90:91], v[88:89], v[90:91]
	v_rcp_f32_e32 v94, v94
	v_rcp_f32_e32 v95, v95
	v_pk_fma_f32 v[92:93], v[92:93], v[88:89], v[92:93]
	v_pk_fma_f32 v[92:93], v[40:41], v[90:91], v[92:93]
	v_exp_f32_e32 v96, v53
	v_pk_mul_f32 v[40:41], v[92:93], v[94:95]
	v_exp_f32_e32 v98, v40
	v_exp_f32_e32 v99, v41
	v_exp_f32_e32 v97, v57
	v_pk_add_f32 v[100:101], v[98:99], 1.0 op_sel_hi:[1,0]
	v_pk_fma_f32 v[100:101], v[100:101], v[96:97], v[100:101]
	v_rcp_f32_e32 v100, v100
	v_rcp_f32_e32 v101, v101
	v_pk_add_f32 v[102:103], v[98:99], -1.0 op_sel_hi:[1,0]
	v_pk_mul_f32 v[102:103], v[102:103], v[100:101]
	v_cvt_pk_f16_f32 v104, v102, v103
	ds_write_b32 v79, v104 offset:0
	s_waitcnt lgkmcnt(0)
	s_barrier
	ds_read_b128 v[42:45], v78 offset:0
	ds_read_b128 v[46:49], v78 offset:1024
	v_mfma_f32_16x16x32_f16 v[50:53], v[2:5], v[34:37], v[6:9]
	v_mfma_f32_16x16x32_f16 v[54:57], v[26:29], v[34:37], v[30:33]
	s_waitcnt lgkmcnt(1)
	v_mfma_f32_16x16x32_f16 v[50:53], v[18:21], v[42:45], v[50:53]
	v_mfma_f32_16x16x32_f16 v[54:57], v[10:13], v[42:45], v[54:57]
	s_waitcnt lgkmcnt(0)
	v_mfma_f32_16x16x32_f16 v[50:53], v[22:25], v[46:49], v[50:53]
	v_mfma_f32_16x16x32_f16 v[54:57], v[14:17], v[46:49], v[54:57]
	ds_read_b128 v[34:37], v39 offset:1024
	s_nop 6
	v_exp_f32_e32 v84, v52
	v_exp_f32_e32 v85, v56
	v_exp_f32_e32 v86, v50
	v_exp_f32_e32 v87, v54
	v_exp_f32_e32 v88, v51
	v_exp_f32_e32 v89, v55
	v_pk_add_f32 v[90:91], v[84:85], 1.0 op_sel_hi:[1,0]
	v_pk_fma_f32 v[92:93], v[84:85], s[0:1], v[58:59] op_sel_hi:[1,0,0]
	v_pk_fma_f32 v[90:91], v[86:87], v[90:91], v[90:91]
	v_pk_fma_f32 v[94:95], v[90:91], v[88:89], v[90:91]
	v_rcp_f32_e32 v94, v94
	v_rcp_f32_e32 v95, v95
	v_pk_fma_f32 v[92:93], v[92:93], v[88:89], v[92:93]
	v_pk_fma_f32 v[92:93], v[40:41], v[90:91], v[92:93]
	v_exp_f32_e32 v96, v53
	v_pk_mul_f32 v[40:41], v[92:93], v[94:95]
	v_exp_f32_e32 v98, v40
	v_exp_f32_e32 v99, v41
	v_exp_f32_e32 v97, v57
	v_pk_add_f32 v[100:101], v[98:99], 1.0 op_sel_hi:[1,0]
	v_pk_fma_f32 v[100:101], v[100:101], v[96:97], v[100:101]
	v_rcp_f32_e32 v100, v100
	v_rcp_f32_e32 v101, v101
	v_pk_add_f32 v[102:103], v[98:99], -1.0 op_sel_hi:[1,0]
	v_pk_mul_f32 v[102:103], v[102:103], v[100:101]
	v_cvt_pk_f16_f32 v104, v102, v103
	ds_write_b32 v79, v104 offset:2048
	s_waitcnt lgkmcnt(0)
	s_add_u32 s9, s9, 4
	v_add_u32_e32 v39, 0x400, v39
	s_cmp_lt_u32 s9, 450
	s_cbranch_scc1 .Lpa_loop
	s_barrier
	s_endpgm
